# m2 (scan loop rewrite, XP5 96, 3-deep hand-written w_down converter for the gate/up-phase converter workgroups) + phase-1 partials reduction with all 32 loads in flight
# speedup vs baseline: 1.0066x; 1.0015x over previous
; #define LAS __attribute__((address_space(3)))
; __device__ __forceinline__ void phase1(const Params& p, LAS unsigned char* lds, const int wave) {
;     const int tid = phase_tid(wave);
;     const int bid = blockIdx.x;
;     if (tid < 192) { const int idx = bid * 192 + tid, b = idx / NMOD, j = idx % NMOD; float s = p.b_ada[j];
;         for (int ks = 0; ks < KS_MOD; ++ks) s += p.modp[(size_t)(ks * 4 + b) * NMOD + j];
;         p.mod[idx] = s; }
.LBB0_81:
	s_or_b64 exec, exec, s[0:1]
	v_readlane_b32 s0, v254, 2
	s_lshr_b32 s0, s0, 6
	s_waitcnt lgkmcnt(0)
	v_writelane_b32 v255, s0, 30
	s_barrier
	v_mbcnt_lo_u32_b32 v0, -1, 0
	v_mbcnt_hi_u32_b32 v0, -1, v0
	s_movk_i32 s0, 0xc0
	v_add_u32_e32 v22, s91, v0
	v_cmp_gt_i32_e32 vcc, s0, v22
	s_and_saveexec_b64 s[4:5], vcc
	s_cbranch_execz .LBB0_85
	v_readlane_b32 s0, v254, 3
	s_mulk_i32 s0, 0xc0
	v_readlane_b32 s12, v254, 40
	v_add_u32_e32 v0, s0, v22
	s_mov_b32 s0, 0x2aaaaaab
	v_mul_hi_i32 v1, v0, s0
	v_lshrrev_b32_e32 v2, 31, v1
	v_ashrrev_i32_e32 v1, 11, v1
	v_add_u32_e32 v1, v1, v2
	v_mul_i32_i24_e32 v2, 0x3000, v1
	v_sub_u32_e32 v2, v0, v2
	v_ashrrev_i32_e32 v3, 31, v2
	v_lshlrev_b64 v[2:3], 2, v[2:3]
	v_readlane_b32 s18, v254, 46
	v_readlane_b32 s19, v254, 47
	v_readlane_b32 s13, v254, 41
	v_readlane_b32 s14, v254, 42
	v_lshl_add_u64 v[4:5], s[18:19], 0, v[2:3]
	global_load_dword v4, v[4:5], off
	v_readlane_b32 s15, v254, 43
	v_readlane_b32 s16, v254, 44
	v_readlane_b32 s17, v254, 45
	v_readlane_b32 s20, v254, 48
	v_readlane_b32 s21, v254, 49
	v_readlane_b32 s22, v254, 50
	v_readlane_b32 s23, v254, 51
	v_readlane_b32 s24, v254, 52
	v_readlane_b32 s25, v254, 53
	v_readlane_b32 s26, v254, 54
	v_readlane_b32 s27, v254, 55
	v_readlane_b32 s1, v254, 4
	s_mov_b32 s0, 0xc000
	v_readlane_b32 s12, v254, 5
	v_mad_i64_i32 v[2:3], s[0:1], v1, s0, v[2:3]
	v_readlane_b32 s14, v254, 7
	v_readlane_b32 s15, v254, 8
	s_mov_b64 s[6:7], 0
	v_readlane_b32 s13, v254, 6
	v_lshl_add_u64 v[2:3], s[14:15], 0, v[2:3]
	v_readlane_b32 s16, v254, 9
	v_readlane_b32 s17, v254, 10
	v_readlane_b32 s18, v254, 11
	v_readlane_b32 s19, v254, 12
	v_readlane_b32 s20, v254, 13
	v_readlane_b32 s21, v254, 14
	v_readlane_b32 s22, v254, 15
	v_readlane_b32 s23, v254, 16
	v_readlane_b32 s24, v254, 17
	v_readlane_b32 s25, v254, 18
	v_readlane_b32 s26, v254, 19
	v_readlane_b32 s27, v254, 20
	global_load_dword v32, v[2:3], off
	s_mov_b32 s0, 0x30000
	s_mov_b32 s1, 0
	v_lshl_add_u64 v[24:25], v[2:3], 0, s[0:1]
	global_load_dword v33, v[24:25], off
	s_mov_b32 s0, 0x60000
	s_mov_b32 s1, 0
	v_lshl_add_u64 v[24:25], v[2:3], 0, s[0:1]
	global_load_dword v34, v[24:25], off
	s_mov_b32 s0, 0x90000
	s_mov_b32 s1, 0
	v_lshl_add_u64 v[24:25], v[2:3], 0, s[0:1]
	global_load_dword v35, v[24:25], off
	s_mov_b32 s0, 0xc0000
	s_mov_b32 s1, 0
	v_lshl_add_u64 v[24:25], v[2:3], 0, s[0:1]
	global_load_dword v36, v[24:25], off
	s_mov_b32 s0, 0xf0000
	s_mov_b32 s1, 0
	v_lshl_add_u64 v[24:25], v[2:3], 0, s[0:1]
	global_load_dword v37, v[24:25], off
	s_mov_b32 s0, 0x120000
	s_mov_b32 s1, 0
	v_lshl_add_u64 v[24:25], v[2:3], 0, s[0:1]
	global_load_dword v38, v[24:25], off
	s_mov_b32 s0, 0x150000
	s_mov_b32 s1, 0
	v_lshl_add_u64 v[24:25], v[2:3], 0, s[0:1]
	global_load_dword v39, v[24:25], off
	s_mov_b32 s0, 0x180000
	s_mov_b32 s1, 0
	v_lshl_add_u64 v[24:25], v[2:3], 0, s[0:1]
	global_load_dword v40, v[24:25], off
	s_mov_b32 s0, 0x1b0000
	s_mov_b32 s1, 0
	v_lshl_add_u64 v[24:25], v[2:3], 0, s[0:1]
	global_load_dword v41, v[24:25], off
	s_mov_b32 s0, 0x1e0000
	s_mov_b32 s1, 0
	v_lshl_add_u64 v[24:25], v[2:3], 0, s[0:1]
	global_load_dword v42, v[24:25], off
	s_mov_b32 s0, 0x210000
	s_mov_b32 s1, 0
	v_lshl_add_u64 v[24:25], v[2:3], 0, s[0:1]
	global_load_dword v43, v[24:25], off
	s_mov_b32 s0, 0x240000
	s_mov_b32 s1, 0
	v_lshl_add_u64 v[24:25], v[2:3], 0, s[0:1]
	global_load_dword v44, v[24:25], off
	s_mov_b32 s0, 0x270000
	s_mov_b32 s1, 0
	v_lshl_add_u64 v[24:25], v[2:3], 0, s[0:1]
	global_load_dword v45, v[24:25], off
	s_mov_b32 s0, 0x2a0000
	s_mov_b32 s1, 0
	v_lshl_add_u64 v[24:25], v[2:3], 0, s[0:1]
	global_load_dword v46, v[24:25], off
	s_mov_b32 s0, 0x2d0000
	s_mov_b32 s1, 0
	v_lshl_add_u64 v[24:25], v[2:3], 0, s[0:1]
	global_load_dword v47, v[24:25], off
	s_mov_b32 s0, 0x300000
	s_mov_b32 s1, 0
	v_lshl_add_u64 v[24:25], v[2:3], 0, s[0:1]
	global_load_dword v48, v[24:25], off
	s_mov_b32 s0, 0x330000
	s_mov_b32 s1, 0
	v_lshl_add_u64 v[24:25], v[2:3], 0, s[0:1]
	global_load_dword v49, v[24:25], off
	s_mov_b32 s0, 0x360000
	s_mov_b32 s1, 0
	v_lshl_add_u64 v[24:25], v[2:3], 0, s[0:1]
	global_load_dword v50, v[24:25], off
	s_mov_b32 s0, 0x390000
	s_mov_b32 s1, 0
	v_lshl_add_u64 v[24:25], v[2:3], 0, s[0:1]
	global_load_dword v51, v[24:25], off
	s_mov_b32 s0, 0x3c0000
	s_mov_b32 s1, 0
	v_lshl_add_u64 v[24:25], v[2:3], 0, s[0:1]
	global_load_dword v52, v[24:25], off
	s_mov_b32 s0, 0x3f0000
	s_mov_b32 s1, 0
	v_lshl_add_u64 v[24:25], v[2:3], 0, s[0:1]
	global_load_dword v53, v[24:25], off
	s_mov_b32 s0, 0x420000
	s_mov_b32 s1, 0
	v_lshl_add_u64 v[24:25], v[2:3], 0, s[0:1]
	global_load_dword v54, v[24:25], off
	s_mov_b32 s0, 0x450000
	s_mov_b32 s1, 0
	v_lshl_add_u64 v[24:25], v[2:3], 0, s[0:1]
	global_load_dword v55, v[24:25], off
	s_mov_b32 s0, 0x480000
	s_mov_b32 s1, 0
	v_lshl_add_u64 v[24:25], v[2:3], 0, s[0:1]
	global_load_dword v56, v[24:25], off
	s_mov_b32 s0, 0x4b0000
	s_mov_b32 s1, 0
	v_lshl_add_u64 v[24:25], v[2:3], 0, s[0:1]
	global_load_dword v57, v[24:25], off
	s_mov_b32 s0, 0x4e0000
	s_mov_b32 s1, 0
	v_lshl_add_u64 v[24:25], v[2:3], 0, s[0:1]
	global_load_dword v58, v[24:25], off
	s_mov_b32 s0, 0x510000
	s_mov_b32 s1, 0
	v_lshl_add_u64 v[24:25], v[2:3], 0, s[0:1]
	global_load_dword v59, v[24:25], off
	s_mov_b32 s0, 0x540000
	s_mov_b32 s1, 0
	v_lshl_add_u64 v[24:25], v[2:3], 0, s[0:1]
	global_load_dword v60, v[24:25], off
	s_mov_b32 s0, 0x570000
	s_mov_b32 s1, 0
	v_lshl_add_u64 v[24:25], v[2:3], 0, s[0:1]
	global_load_dword v61, v[24:25], off
	s_mov_b32 s0, 0x5a0000
	s_mov_b32 s1, 0
	v_lshl_add_u64 v[24:25], v[2:3], 0, s[0:1]
	global_load_dword v62, v[24:25], off
	s_mov_b32 s0, 0x5d0000
	s_mov_b32 s1, 0
	v_lshl_add_u64 v[24:25], v[2:3], 0, s[0:1]
	global_load_dword v63, v[24:25], off
	s_waitcnt vmcnt(31)
; __device__ __forceinline__ void phase1(const Params& p, LAS unsigned char* lds, const int wave) {
;     ...
;     if (tid < 192) { const int idx = bid * 192 + tid, b = idx / NMOD, j = idx % NMOD; float s = p.b_ada[j];
;         for (int ks = 0; ks < KS_MOD; ++ks) s += p.modp[(size_t)(ks * 4 + b) * NMOD + j];
;         p.mod[idx] = s; }
	v_add_f32_e32 v4, v4, v32
	s_waitcnt vmcnt(30)
	v_add_f32_e32 v4, v4, v33
	s_waitcnt vmcnt(29)
	v_add_f32_e32 v4, v4, v34
	s_waitcnt vmcnt(28)
	v_add_f32_e32 v4, v4, v35
	s_waitcnt vmcnt(27)
	v_add_f32_e32 v4, v4, v36
	s_waitcnt vmcnt(26)
	v_add_f32_e32 v4, v4, v37
	s_waitcnt vmcnt(25)
	v_add_f32_e32 v4, v4, v38
	s_waitcnt vmcnt(24)
	v_add_f32_e32 v4, v4, v39
	s_waitcnt vmcnt(23)
	v_add_f32_e32 v4, v4, v40
	s_waitcnt vmcnt(22)
	v_add_f32_e32 v4, v4, v41
	s_waitcnt vmcnt(21)
	v_add_f32_e32 v4, v4, v42
	s_waitcnt vmcnt(20)
	v_add_f32_e32 v4, v4, v43
	s_waitcnt vmcnt(19)
	v_add_f32_e32 v4, v4, v44
	s_waitcnt vmcnt(18)
	v_add_f32_e32 v4, v4, v45
	s_waitcnt vmcnt(17)
	v_add_f32_e32 v4, v4, v46
	s_waitcnt vmcnt(16)
	v_add_f32_e32 v4, v4, v47
	s_waitcnt vmcnt(15)
	v_add_f32_e32 v4, v4, v48
	s_waitcnt vmcnt(14)
	v_add_f32_e32 v4, v4, v49
	s_waitcnt vmcnt(13)
	v_add_f32_e32 v4, v4, v50
	s_waitcnt vmcnt(12)
	v_add_f32_e32 v4, v4, v51
	s_waitcnt vmcnt(11)
	v_add_f32_e32 v4, v4, v52
	s_waitcnt vmcnt(10)
	v_add_f32_e32 v4, v4, v53
	s_waitcnt vmcnt(9)
	v_add_f32_e32 v4, v4, v54
	s_waitcnt vmcnt(8)
	v_add_f32_e32 v4, v4, v55
	s_waitcnt vmcnt(7)
	v_add_f32_e32 v4, v4, v56
	s_waitcnt vmcnt(6)
	v_add_f32_e32 v4, v4, v57
	s_waitcnt vmcnt(5)
	v_add_f32_e32 v4, v4, v58
	s_waitcnt vmcnt(4)
	v_add_f32_e32 v4, v4, v59
	s_waitcnt vmcnt(3)
	v_add_f32_e32 v4, v4, v60
	s_waitcnt vmcnt(2)
	v_add_f32_e32 v4, v4, v61
	s_waitcnt vmcnt(1)
	v_add_f32_e32 v4, v4, v62
	s_waitcnt vmcnt(0)
	v_add_f32_e32 v4, v4, v63
	v_readlane_b32 s36, v254, 5
	v_ashrrev_i32_e32 v1, 31, v0
	v_readlane_b32 s40, v254, 9
	v_readlane_b32 s41, v254, 10
	v_readlane_b32 s37, v254, 6
	v_readlane_b32 s38, v254, 7
	v_lshl_add_u64 v[0:1], v[0:1], 2, s[40:41]
	v_readlane_b32 s39, v254, 8
	v_readlane_b32 s42, v254, 11
	v_readlane_b32 s43, v254, 12
	v_readlane_b32 s44, v254, 13
	v_readlane_b32 s45, v254, 14
	v_readlane_b32 s46, v254, 15
	v_readlane_b32 s47, v254, 16
	v_readlane_b32 s48, v254, 17
	v_readlane_b32 s49, v254, 18
	v_readlane_b32 s50, v254, 19
	v_readlane_b32 s51, v254, 20
	global_store_dword v[0:1], v4, off

; #define LAS __attribute__((address_space(3)))
; __device__ __forceinline__ void cvt_item_lds(const float* src, int ld_src, fp8_t* dst, int ld_dst, LAS unsigned char* lds, int tid, int wv) {
;     const int lane = tid & 63;
;     const float* s = src + (size_t)(16 * wv) * ld_src + 4 * lane;
;     f32x4 va[16], vb[16];
;     cvt8_load(va, s, ld_src);
; #pragma unroll
;     for (int t = 0; t < 8; t += 2) {
;         cvt8_load(vb, s + (t + 1) * 256, ld_src); __builtin_amdgcn_sched_barrier(0);
; __device__ __forceinline__ void conv_queue(const Params& p, LAS unsigned char* lds, const int wave, const int cw, const int first, const int last, const int slot_off = LDS_MISC) {
;     ...
;     for (;;) {
;         __syncthreads();
;         if (tid == 0) *slot = first + (int)atomicAdd(&p.ctl[cw], 1u);
;         __syncthreads();
;         const int it = *slot;
;         if (it >= last) break;
;         if (it < N_GU) { const int e = it >> 5, rem = it & 31, kb = rem >> 1, nh = rem & 1;
;             const float* src = p.w_gu + (size_t)e * ND * (2 * DFF) + (size_t)(kb * 128) * (2 * DFF) + nh * 2048;
;             fp8_t* dst = p.wt_gu + (size_t)e * (2 * DFF) * ND + (size_t)(nh * 2048) * ND + kb * 128;
;             cvt_item_lds(src, 2 * DFF, dst, ND, lds, tid, wave); }
;         else { const int j = it - N_GU, e = j >> 4, kb = j & 15;
;             const float* src = p.w_down + (size_t)e * DFF * ND + (size_t)(kb * 128) * ND;
;             fp8_t* dst = p.wt_down + (size_t)e * ND * DFF + kb * 128;
;             cvt_item_lds(src, ND, dst, DFF, lds, tid, wave); }
.LBB0_1252:
	s_or_b64 exec, exec, s[50:51]
	s_waitcnt lgkmcnt(0)
	s_barrier
	ds_read_b32 v0, v204
	s_movk_i32 s2, 0x59f
	s_mov_b64 s[50:51], -1
	s_waitcnt lgkmcnt(0)
	v_cmp_lt_i32_e32 vcc, s2, v0
	v_readfirstlane_b32 s33, v0
	s_cbranch_vccnz .LBB0_1247
	s_cmpk_gt_i32 s33, 0x3ff
	s_cbranch_scc0 .LBB0_1255
	s_add_i32 s2, s33, 0xfffffc00
	v_readlane_b32 s52, v254, 26
	v_readlane_b32 s53, v254, 27
	s_lshr_b32 s4, s2, 4
	s_lshl_b64 s[34:35], s[4:5], 22
	s_add_u32 s34, s56, s34
	s_addc_u32 s35, s57, s35
	s_lshl_b32 s50, s33, 7
	s_and_b32 s50, s50, 0x780
	s_add_u32 s64, s34, s50
	s_addc_u32 s65, s35, 0
	s_lshr_b32 s51, s2, 12
	s_lshl_b32 s50, s2, 20
	s_add_u32 s50, s50, s52
	s_addc_u32 s51, s51, s53
	s_add_u32 s16, s50, s14
	s_addc_u32 s17, s51, s15
	s_add_u32 s18, s16, 0x2000
	s_addc_u32 s19, s17, 0
	s_add_u32 s20, s18, 0x2000
	s_addc_u32 s21, s19, 0
	s_add_u32 s22, s20, 0x2000
	s_addc_u32 s23, s21, 0
	s_add_u32 s24, s22, 0x2000
	s_addc_u32 s25, s23, 0
	s_add_u32 s26, s24, 0x2000
	s_addc_u32 s27, s25, 0
	s_add_u32 s28, s26, 0x2000
	s_addc_u32 s29, s27, 0
	s_add_u32 s30, s28, 0x2000
	s_addc_u32 s31, s29, 0
	s_add_u32 s38, s30, 0x2000
	s_addc_u32 s39, s31, 0
	s_add_u32 s40, s38, 0x2000
	s_addc_u32 s41, s39, 0
	s_add_u32 s42, s40, 0x2000
	s_addc_u32 s43, s41, 0
	s_add_u32 s44, s42, 0x2000
	s_addc_u32 s45, s43, 0
	s_add_u32 s46, s44, 0x2000
	s_addc_u32 s47, s45, 0
	s_add_u32 s48, s46, 0x2000
	s_addc_u32 s49, s47, 0
	s_add_u32 s60, s48, 0x2000
	s_addc_u32 s61, s49, 0
	s_add_u32 s62, s60, 0x2000
	s_addc_u32 s63, s61, 0
	global_load_dwordx4 v[0:3], v136, s[16:17] nt
	global_load_dwordx4 v[4:7], v136, s[18:19] nt
	global_load_dwordx4 v[8:11], v136, s[20:21] nt
	global_load_dwordx4 v[12:15], v136, s[22:23] nt
	global_load_dwordx4 v[16:19], v136, s[24:25] nt
	global_load_dwordx4 v[20:23], v136, s[26:27] nt
	global_load_dwordx4 v[24:27], v136, s[28:29] nt
	global_load_dwordx4 v[28:31], v136, s[30:31] nt
	global_load_dwordx4 v[32:35], v136, s[38:39] nt
	global_load_dwordx4 v[36:39], v136, s[40:41] nt
	global_load_dwordx4 v[40:43], v136, s[42:43] nt
	global_load_dwordx4 v[44:47], v136, s[44:45] nt
	global_load_dwordx4 v[48:51], v136, s[46:47] nt
	global_load_dwordx4 v[52:55], v136, s[48:49] nt
	global_load_dwordx4 v[56:59], v136, s[60:61] nt
	global_load_dwordx4 v[60:63], v136, s[62:63] nt
	global_load_dwordx4 v[64:67], v136, s[16:17] offset:1024 nt
	global_load_dwordx4 v[68:71], v136, s[18:19] offset:1024 nt
	global_load_dwordx4 v[72:75], v136, s[20:21] offset:1024 nt
	global_load_dwordx4 v[76:79], v136, s[22:23] offset:1024 nt
	global_load_dwordx4 v[80:83], v136, s[24:25] offset:1024 nt
	global_load_dwordx4 v[84:87], v136, s[26:27] offset:1024 nt
	global_load_dwordx4 v[88:91], v136, s[28:29] offset:1024 nt
	global_load_dwordx4 v[92:95], v136, s[30:31] offset:1024 nt
	global_load_dwordx4 v[96:99], v136, s[38:39] offset:1024 nt
	global_load_dwordx4 v[100:103], v136, s[40:41] offset:1024 nt
	global_load_dwordx4 v[104:107], v136, s[42:43] offset:1024 nt
	global_load_dwordx4 v[108:111], v136, s[44:45] offset:1024 nt
	global_load_dwordx4 v[112:115], v136, s[46:47] offset:1024 nt
	global_load_dwordx4 v[116:119], v136, s[48:49] offset:1024 nt
	global_load_dwordx4 v[120:123], v136, s[60:61] offset:1024 nt
	global_load_dwordx4 v[124:127], v136, s[62:63] offset:1024 nt
	global_load_dwordx4 v[128:131], v136, s[16:17] offset:2048 nt
	global_load_dwordx4 v[132:135], v136, s[18:19] offset:2048 nt
	global_load_dwordx4 v[148:151], v136, s[20:21] offset:2048 nt
	global_load_dwordx4 v[152:155], v136, s[22:23] offset:2048 nt
	global_load_dwordx4 v[156:159], v136, s[24:25] offset:2048 nt
	global_load_dwordx4 v[160:163], v136, s[26:27] offset:2048 nt
	global_load_dwordx4 v[164:167], v136, s[28:29] offset:2048 nt
	global_load_dwordx4 v[168:171], v136, s[30:31] offset:2048 nt
	global_load_dwordx4 v[172:175], v136, s[38:39] offset:2048 nt
	global_load_dwordx4 v[176:179], v136, s[40:41] offset:2048 nt
	global_load_dwordx4 v[180:183], v136, s[42:43] offset:2048 nt
	global_load_dwordx4 v[184:187], v136, s[44:45] offset:2048 nt
	global_load_dwordx4 v[188:191], v136, s[46:47] offset:2048 nt
	global_load_dwordx4 v[192:195], v136, s[48:49] offset:2048 nt
	global_load_dwordx4 v[196:199], v136, s[60:61] offset:2048 nt
	global_load_dwordx4 v[200:203], v136, s[62:63] offset:2048 nt
	s_waitcnt vmcnt(32)
; #define LAS __attribute__((address_space(3)))
; __device__ __forceinline__ unsigned pack4_fp8(float a, float b, float c, float d) { int r = 0; r = __builtin_amdgcn_cvt_pk_fp8_f32(a, b, r, false); r = __builtin_amdgcn_cvt_pk_fp8_f32(c, d, r, true); return (unsigned)r; }
; __device__ __forceinline__ void cvt8_to_lds(const f32x4 (&v)[16], LAS unsigned char* tile, int lane, int wv) {
; #pragma unroll
;     for (int i = 0; i < 4; ++i) { u32x4 w; w.x = pack4_fp8(v[0][i] * W8_SCALE, v[1][i] * W8_SCALE, v[2][i] * W8_SCALE, v[3][i] * W8_SCALE); w.y = pack4_fp8(v[4][i] * W8_SCALE, v[5][i] * W8_SCALE, v[6][i] * W8_SCALE, v[7][i] * W8_SCALE);
;         w.z = pack4_fp8(v[8][i] * W8_SCALE, v[9][i] * W8_SCALE, v[10][i] * W8_SCALE, v[11][i] * W8_SCALE); w.w = pack4_fp8(v[12][i] * W8_SCALE, v[13][i] * W8_SCALE, v[14][i] * W8_SCALE, v[15][i] * W8_SCALE);
;         *(LAS u32x4*)(tile + (4 * lane + i) * 128 + ((wv ^ (lane & 7)) << 4)) = w; }
; }
; __device__ __forceinline__ void cvt8_from_lds(const LAS unsigned char* tile, fp8_t* d, int ld_dst, int tid) {
;     const int c = tid & 7;
; #pragma unroll
;     for (int q = 0; q < 4; ++q) { const int r = (tid >> 3) + 64 * q; const u32x4 w = *(const LAS u32x4*)(tile + r * 128 + ((c ^ ((r >> 2) & 7)) << 4));
;         __builtin_nontemporal_store(w, (u32x4*)(d + (size_t)r * ld_dst + 16 * c)); }
; }
; __device__ __forceinline__ void cvt_item_lds(const float* src, int ld_src, fp8_t* dst, int ld_dst, LAS unsigned char* lds, int tid, int wv) {
;     const int lane = tid & 63;
;     const float* s = src + (size_t)(16 * wv) * ld_src + 4 * lane;
;     f32x4 va[16], vb[16];
;     cvt8_load(va, s, ld_src);
; #pragma unroll
;     for (int t = 0; t < 8; t += 2) {
;         cvt8_load(vb, s + (t + 1) * 256, ld_src); __builtin_amdgcn_sched_barrier(0);
;         cvt8_to_lds(va, lds, lane, wv); CVT_LDS_BAR(); __builtin_amdgcn_sched_barrier(0);
;         cvt8_from_lds(lds, dst + (size_t)(t * 256) * ld_dst, ld_dst, tid); __builtin_amdgcn_sched_barrier(0);
;         if (t + 2 < 8) { cvt8_load(va, s + (t + 2) * 256, ld_src); __builtin_amdgcn_sched_barrier(0); }
;         cvt8_to_lds(vb, lds + 32768, lane, wv); CVT_LDS_BAR(); __builtin_amdgcn_sched_barrier(0);
;         cvt8_from_lds(lds + 32768, dst + (size_t)((t + 1) * 256) * ld_dst, ld_dst, tid); __builtin_amdgcn_sched_barrier(0);
;     }
	v_mul_f32_e32 v0, 0x42800000, v0
	v_mul_f32_e32 v4, 0x42800000, v4
	v_mul_f32_e32 v8, 0x42800000, v8
	v_mul_f32_e32 v12, 0x42800000, v12
	v_mul_f32_e32 v16, 0x42800000, v16
	v_mul_f32_e32 v20, 0x42800000, v20
	v_mul_f32_e32 v24, 0x42800000, v24
	v_mul_f32_e32 v28, 0x42800000, v28
	v_mul_f32_e32 v32, 0x42800000, v32
	v_mul_f32_e32 v36, 0x42800000, v36
	v_mul_f32_e32 v40, 0x42800000, v40
	v_mul_f32_e32 v44, 0x42800000, v44
	v_mul_f32_e32 v48, 0x42800000, v48
	v_mul_f32_e32 v52, 0x42800000, v52
	v_mul_f32_e32 v56, 0x42800000, v56
	v_mul_f32_e32 v60, 0x42800000, v60
	v_cvt_pk_fp8_f32 v210, v0, v4
	v_cvt_pk_fp8_f32 v211, v16, v20
	v_cvt_pk_fp8_f32 v212, v32, v36
	v_cvt_pk_fp8_f32 v213, v48, v52
	v_cvt_pk_fp8_f32 v210, v8, v12 op_sel:[0,0,1]
	v_cvt_pk_fp8_f32 v211, v24, v28 op_sel:[0,0,1]
	v_cvt_pk_fp8_f32 v212, v40, v44 op_sel:[0,0,1]
	v_cvt_pk_fp8_f32 v213, v56, v60 op_sel:[0,0,1]
	ds_write_b128 v205, v[210:213] offset:0
	v_mul_f32_e32 v1, 0x42800000, v1
	v_mul_f32_e32 v5, 0x42800000, v5
	v_mul_f32_e32 v9, 0x42800000, v9
	v_mul_f32_e32 v13, 0x42800000, v13
	v_mul_f32_e32 v17, 0x42800000, v17
	v_mul_f32_e32 v21, 0x42800000, v21
	v_mul_f32_e32 v25, 0x42800000, v25
	v_mul_f32_e32 v29, 0x42800000, v29
	v_mul_f32_e32 v33, 0x42800000, v33
	v_mul_f32_e32 v37, 0x42800000, v37
	v_mul_f32_e32 v41, 0x42800000, v41
	v_mul_f32_e32 v45, 0x42800000, v45
	v_mul_f32_e32 v49, 0x42800000, v49
	v_mul_f32_e32 v53, 0x42800000, v53
	v_mul_f32_e32 v57, 0x42800000, v57
	v_mul_f32_e32 v61, 0x42800000, v61
	v_cvt_pk_fp8_f32 v210, v1, v5
	v_cvt_pk_fp8_f32 v211, v17, v21
	v_cvt_pk_fp8_f32 v212, v33, v37
	v_cvt_pk_fp8_f32 v213, v49, v53
	v_cvt_pk_fp8_f32 v210, v9, v13 op_sel:[0,0,1]
	v_cvt_pk_fp8_f32 v211, v25, v29 op_sel:[0,0,1]
	v_cvt_pk_fp8_f32 v212, v41, v45 op_sel:[0,0,1]
	v_cvt_pk_fp8_f32 v213, v57, v61 op_sel:[0,0,1]
	ds_write_b128 v205, v[210:213] offset:128
	v_mul_f32_e32 v2, 0x42800000, v2
	v_mul_f32_e32 v6, 0x42800000, v6
	v_mul_f32_e32 v10, 0x42800000, v10
	v_mul_f32_e32 v14, 0x42800000, v14
	v_mul_f32_e32 v18, 0x42800000, v18
	v_mul_f32_e32 v22, 0x42800000, v22
	v_mul_f32_e32 v26, 0x42800000, v26
	v_mul_f32_e32 v30, 0x42800000, v30
	v_mul_f32_e32 v34, 0x42800000, v34
	v_mul_f32_e32 v38, 0x42800000, v38
	v_mul_f32_e32 v42, 0x42800000, v42
	v_mul_f32_e32 v46, 0x42800000, v46
	v_mul_f32_e32 v50, 0x42800000, v50
	v_mul_f32_e32 v54, 0x42800000, v54
	v_mul_f32_e32 v58, 0x42800000, v58
	v_mul_f32_e32 v62, 0x42800000, v62
	v_cvt_pk_fp8_f32 v210, v2, v6
	v_cvt_pk_fp8_f32 v211, v18, v22
	v_cvt_pk_fp8_f32 v212, v34, v38
	v_cvt_pk_fp8_f32 v213, v50, v54
	v_cvt_pk_fp8_f32 v210, v10, v14 op_sel:[0,0,1]
	v_cvt_pk_fp8_f32 v211, v26, v30 op_sel:[0,0,1]
	v_cvt_pk_fp8_f32 v212, v42, v46 op_sel:[0,0,1]
	v_cvt_pk_fp8_f32 v213, v58, v62 op_sel:[0,0,1]
	ds_write_b128 v205, v[210:213] offset:256
	v_mul_f32_e32 v3, 0x42800000, v3
	v_mul_f32_e32 v7, 0x42800000, v7
	v_mul_f32_e32 v11, 0x42800000, v11
	v_mul_f32_e32 v15, 0x42800000, v15
	v_mul_f32_e32 v19, 0x42800000, v19
	v_mul_f32_e32 v23, 0x42800000, v23
	v_mul_f32_e32 v27, 0x42800000, v27
	v_mul_f32_e32 v31, 0x42800000, v31
	v_mul_f32_e32 v35, 0x42800000, v35
	v_mul_f32_e32 v39, 0x42800000, v39
	v_mul_f32_e32 v43, 0x42800000, v43
	v_mul_f32_e32 v47, 0x42800000, v47
	v_mul_f32_e32 v51, 0x42800000, v51
	v_mul_f32_e32 v55, 0x42800000, v55
	v_mul_f32_e32 v59, 0x42800000, v59
	v_mul_f32_e32 v63, 0x42800000, v63
	v_cvt_pk_fp8_f32 v210, v3, v7
	v_cvt_pk_fp8_f32 v211, v19, v23
	v_cvt_pk_fp8_f32 v212, v35, v39
	v_cvt_pk_fp8_f32 v213, v51, v55
	v_cvt_pk_fp8_f32 v210, v11, v15 op_sel:[0,0,1]
	v_cvt_pk_fp8_f32 v211, v27, v31 op_sel:[0,0,1]
	v_cvt_pk_fp8_f32 v212, v43, v47 op_sel:[0,0,1]
	v_cvt_pk_fp8_f32 v213, v59, v63 op_sel:[0,0,1]
	ds_write_b128 v205, v[210:213] offset:384
	s_waitcnt lgkmcnt(0)
	s_barrier
	ds_read_b128 v[0:3], v206
	ds_read_b128 v[4:7], v207
	ds_read_b128 v[8:11], v208
	ds_read_b128 v[12:15], v209
	v_add_u32_e32 v16, v140, v138
	v_add_u32_e32 v17, v142, v138
	v_add_u32_e32 v18, v144, v138
	v_add_u32_e32 v19, v146, v138
	s_waitcnt lgkmcnt(3)
	global_store_dwordx4 v16, v[0:3], s[64:65] nt
	s_waitcnt lgkmcnt(2)
	global_store_dwordx4 v17, v[4:7], s[64:65] nt
	s_waitcnt lgkmcnt(1)
	global_store_dwordx4 v18, v[8:11], s[64:65] nt
	s_waitcnt lgkmcnt(0)
	global_store_dwordx4 v19, v[12:15], s[64:65] nt
	s_add_u32 s64, s64, 0x80000
	s_addc_u32 s65, s65, 0
	s_nop 1
	global_load_dwordx4 v[0:3], v136, s[16:17] offset:3072 nt
	global_load_dwordx4 v[4:7], v136, s[18:19] offset:3072 nt
	global_load_dwordx4 v[8:11], v136, s[20:21] offset:3072 nt
	global_load_dwordx4 v[12:15], v136, s[22:23] offset:3072 nt
	global_load_dwordx4 v[16:19], v136, s[24:25] offset:3072 nt
	global_load_dwordx4 v[20:23], v136, s[26:27] offset:3072 nt
	global_load_dwordx4 v[24:27], v136, s[28:29] offset:3072 nt
	global_load_dwordx4 v[28:31], v136, s[30:31] offset:3072 nt
	global_load_dwordx4 v[32:35], v136, s[38:39] offset:3072 nt
	global_load_dwordx4 v[36:39], v136, s[40:41] offset:3072 nt
	global_load_dwordx4 v[40:43], v136, s[42:43] offset:3072 nt
	global_load_dwordx4 v[44:47], v136, s[44:45] offset:3072 nt
	global_load_dwordx4 v[48:51], v136, s[46:47] offset:3072 nt
	global_load_dwordx4 v[52:55], v136, s[48:49] offset:3072 nt
	global_load_dwordx4 v[56:59], v136, s[60:61] offset:3072 nt
	global_load_dwordx4 v[60:63], v136, s[62:63] offset:3072 nt
	s_waitcnt vmcnt(36)
; #define LAS __attribute__((address_space(3)))
; __device__ __forceinline__ unsigned pack4_fp8(float a, float b, float c, float d) { int r = 0; r = __builtin_amdgcn_cvt_pk_fp8_f32(a, b, r, false); r = __builtin_amdgcn_cvt_pk_fp8_f32(c, d, r, true); return (unsigned)r; }
; __device__ __forceinline__ void cvt8_to_lds(const f32x4 (&v)[16], LAS unsigned char* tile, int lane, int wv) {
; #pragma unroll
;     for (int i = 0; i < 4; ++i) { u32x4 w; w.x = pack4_fp8(v[0][i] * W8_SCALE, v[1][i] * W8_SCALE, v[2][i] * W8_SCALE, v[3][i] * W8_SCALE); w.y = pack4_fp8(v[4][i] * W8_SCALE, v[5][i] * W8_SCALE, v[6][i] * W8_SCALE, v[7][i] * W8_SCALE);
;         w.z = pack4_fp8(v[8][i] * W8_SCALE, v[9][i] * W8_SCALE, v[10][i] * W8_SCALE, v[11][i] * W8_SCALE); w.w = pack4_fp8(v[12][i] * W8_SCALE, v[13][i] * W8_SCALE, v[14][i] * W8_SCALE, v[15][i] * W8_SCALE);
;         *(LAS u32x4*)(tile + (4 * lane + i) * 128 + ((wv ^ (lane & 7)) << 4)) = w; }
; }
; __device__ __forceinline__ void cvt8_from_lds(const LAS unsigned char* tile, fp8_t* d, int ld_dst, int tid) {
;     const int c = tid & 7;
; #pragma unroll
;     for (int q = 0; q < 4; ++q) { const int r = (tid >> 3) + 64 * q; const u32x4 w = *(const LAS u32x4*)(tile + r * 128 + ((c ^ ((r >> 2) & 7)) << 4));
;         __builtin_nontemporal_store(w, (u32x4*)(d + (size_t)r * ld_dst + 16 * c)); }
; }
; __device__ __forceinline__ void cvt_item_lds(const float* src, int ld_src, fp8_t* dst, int ld_dst, LAS unsigned char* lds, int tid, int wv) {
;     const int lane = tid & 63;
;     const float* s = src + (size_t)(16 * wv) * ld_src + 4 * lane;
;     f32x4 va[16], vb[16];
;     cvt8_load(va, s, ld_src);
; #pragma unroll
;     for (int t = 0; t < 8; t += 2) {
;         cvt8_load(vb, s + (t + 1) * 256, ld_src); __builtin_amdgcn_sched_barrier(0);
;         cvt8_to_lds(va, lds, lane, wv); CVT_LDS_BAR(); __builtin_amdgcn_sched_barrier(0);
;         cvt8_from_lds(lds, dst + (size_t)(t * 256) * ld_dst, ld_dst, tid); __builtin_amdgcn_sched_barrier(0);
;         if (t + 2 < 8) { cvt8_load(va, s + (t + 2) * 256, ld_src); __builtin_amdgcn_sched_barrier(0); }
;         cvt8_to_lds(vb, lds + 32768, lane, wv); CVT_LDS_BAR(); __builtin_amdgcn_sched_barrier(0);
;         cvt8_from_lds(lds + 32768, dst + (size_t)((t + 1) * 256) * ld_dst, ld_dst, tid); __builtin_amdgcn_sched_barrier(0);
;     }
	v_mul_f32_e32 v64, 0x42800000, v64
	v_mul_f32_e32 v68, 0x42800000, v68
	v_mul_f32_e32 v72, 0x42800000, v72
	v_mul_f32_e32 v76, 0x42800000, v76
	v_mul_f32_e32 v80, 0x42800000, v80
	v_mul_f32_e32 v84, 0x42800000, v84
	v_mul_f32_e32 v88, 0x42800000, v88
	v_mul_f32_e32 v92, 0x42800000, v92
	v_mul_f32_e32 v96, 0x42800000, v96
	v_mul_f32_e32 v100, 0x42800000, v100
	v_mul_f32_e32 v104, 0x42800000, v104
	v_mul_f32_e32 v108, 0x42800000, v108
	v_mul_f32_e32 v112, 0x42800000, v112
	v_mul_f32_e32 v116, 0x42800000, v116
	v_mul_f32_e32 v120, 0x42800000, v120
	v_mul_f32_e32 v124, 0x42800000, v124
	v_cvt_pk_fp8_f32 v210, v64, v68
	v_cvt_pk_fp8_f32 v211, v80, v84
	v_cvt_pk_fp8_f32 v212, v96, v100
	v_cvt_pk_fp8_f32 v213, v112, v116
	v_cvt_pk_fp8_f32 v210, v72, v76 op_sel:[0,0,1]
	v_cvt_pk_fp8_f32 v211, v88, v92 op_sel:[0,0,1]
	v_cvt_pk_fp8_f32 v212, v104, v108 op_sel:[0,0,1]
	v_cvt_pk_fp8_f32 v213, v120, v124 op_sel:[0,0,1]
	ds_write_b128 v205, v[210:213] offset:32768
	v_mul_f32_e32 v65, 0x42800000, v65
	v_mul_f32_e32 v69, 0x42800000, v69
	v_mul_f32_e32 v73, 0x42800000, v73
	v_mul_f32_e32 v77, 0x42800000, v77
	v_mul_f32_e32 v81, 0x42800000, v81
	v_mul_f32_e32 v85, 0x42800000, v85
	v_mul_f32_e32 v89, 0x42800000, v89
	v_mul_f32_e32 v93, 0x42800000, v93
	v_mul_f32_e32 v97, 0x42800000, v97
	v_mul_f32_e32 v101, 0x42800000, v101
	v_mul_f32_e32 v105, 0x42800000, v105
	v_mul_f32_e32 v109, 0x42800000, v109
	v_mul_f32_e32 v113, 0x42800000, v113
	v_mul_f32_e32 v117, 0x42800000, v117
	v_mul_f32_e32 v121, 0x42800000, v121
	v_mul_f32_e32 v125, 0x42800000, v125
	v_cvt_pk_fp8_f32 v210, v65, v69
	v_cvt_pk_fp8_f32 v211, v81, v85
	v_cvt_pk_fp8_f32 v212, v97, v101
	v_cvt_pk_fp8_f32 v213, v113, v117
	v_cvt_pk_fp8_f32 v210, v73, v77 op_sel:[0,0,1]
	v_cvt_pk_fp8_f32 v211, v89, v93 op_sel:[0,0,1]
	v_cvt_pk_fp8_f32 v212, v105, v109 op_sel:[0,0,1]
	v_cvt_pk_fp8_f32 v213, v121, v125 op_sel:[0,0,1]
	ds_write_b128 v205, v[210:213] offset:32896
	v_mul_f32_e32 v66, 0x42800000, v66
	v_mul_f32_e32 v70, 0x42800000, v70
	v_mul_f32_e32 v74, 0x42800000, v74
	v_mul_f32_e32 v78, 0x42800000, v78
	v_mul_f32_e32 v82, 0x42800000, v82
	v_mul_f32_e32 v86, 0x42800000, v86
	v_mul_f32_e32 v90, 0x42800000, v90
	v_mul_f32_e32 v94, 0x42800000, v94
	v_mul_f32_e32 v98, 0x42800000, v98
	v_mul_f32_e32 v102, 0x42800000, v102
	v_mul_f32_e32 v106, 0x42800000, v106
	v_mul_f32_e32 v110, 0x42800000, v110
	v_mul_f32_e32 v114, 0x42800000, v114
	v_mul_f32_e32 v118, 0x42800000, v118
	v_mul_f32_e32 v122, 0x42800000, v122
	v_mul_f32_e32 v126, 0x42800000, v126
	v_cvt_pk_fp8_f32 v210, v66, v70
	v_cvt_pk_fp8_f32 v211, v82, v86
	v_cvt_pk_fp8_f32 v212, v98, v102
	v_cvt_pk_fp8_f32 v213, v114, v118
	v_cvt_pk_fp8_f32 v210, v74, v78 op_sel:[0,0,1]
	v_cvt_pk_fp8_f32 v211, v90, v94 op_sel:[0,0,1]
	v_cvt_pk_fp8_f32 v212, v106, v110 op_sel:[0,0,1]
	v_cvt_pk_fp8_f32 v213, v122, v126 op_sel:[0,0,1]
	ds_write_b128 v205, v[210:213] offset:33024
	v_mul_f32_e32 v67, 0x42800000, v67
	v_mul_f32_e32 v71, 0x42800000, v71
	v_mul_f32_e32 v75, 0x42800000, v75
	v_mul_f32_e32 v79, 0x42800000, v79
	v_mul_f32_e32 v83, 0x42800000, v83
	v_mul_f32_e32 v87, 0x42800000, v87
	v_mul_f32_e32 v91, 0x42800000, v91
	v_mul_f32_e32 v95, 0x42800000, v95
	v_mul_f32_e32 v99, 0x42800000, v99
	v_mul_f32_e32 v103, 0x42800000, v103
	v_mul_f32_e32 v107, 0x42800000, v107
	v_mul_f32_e32 v111, 0x42800000, v111
	v_mul_f32_e32 v115, 0x42800000, v115
	v_mul_f32_e32 v119, 0x42800000, v119
	v_mul_f32_e32 v123, 0x42800000, v123
	v_mul_f32_e32 v127, 0x42800000, v127
	v_cvt_pk_fp8_f32 v210, v67, v71
	v_cvt_pk_fp8_f32 v211, v83, v87
	v_cvt_pk_fp8_f32 v212, v99, v103
	v_cvt_pk_fp8_f32 v213, v115, v119
	v_cvt_pk_fp8_f32 v210, v75, v79 op_sel:[0,0,1]
	v_cvt_pk_fp8_f32 v211, v91, v95 op_sel:[0,0,1]
	v_cvt_pk_fp8_f32 v212, v107, v111 op_sel:[0,0,1]
	v_cvt_pk_fp8_f32 v213, v123, v127 op_sel:[0,0,1]
	ds_write_b128 v205, v[210:213] offset:33152
	s_waitcnt lgkmcnt(0)
	s_barrier
	ds_read_b128 v[64:67], v206 offset:32768
	ds_read_b128 v[68:71], v207 offset:32768
	ds_read_b128 v[72:75], v208 offset:32768
	ds_read_b128 v[76:79], v209 offset:32768
	v_add_u32_e32 v80, v140, v138
	v_add_u32_e32 v81, v142, v138
	v_add_u32_e32 v82, v144, v138
	v_add_u32_e32 v83, v146, v138
	s_waitcnt lgkmcnt(3)
	global_store_dwordx4 v80, v[64:67], s[64:65] nt
	s_waitcnt lgkmcnt(2)
	global_store_dwordx4 v81, v[68:71], s[64:65] nt
	s_waitcnt lgkmcnt(1)
	global_store_dwordx4 v82, v[72:75], s[64:65] nt
	s_waitcnt lgkmcnt(0)
	global_store_dwordx4 v83, v[76:79], s[64:65] nt
	s_add_u32 s64, s64, 0x80000
	s_addc_u32 s65, s65, 0
	s_nop 1
	s_add_u32 s16, s16, 0x1000
	s_addc_u32 s17, s17, 0
	s_add_u32 s18, s18, 0x1000
	s_addc_u32 s19, s19, 0
	s_add_u32 s20, s20, 0x1000
	s_addc_u32 s21, s21, 0
	s_add_u32 s22, s22, 0x1000
	s_addc_u32 s23, s23, 0
	s_add_u32 s24, s24, 0x1000
	s_addc_u32 s25, s25, 0
	s_add_u32 s26, s26, 0x1000
	s_addc_u32 s27, s27, 0
	s_add_u32 s28, s28, 0x1000
	s_addc_u32 s29, s29, 0
	s_add_u32 s30, s30, 0x1000
	s_addc_u32 s31, s31, 0
	s_add_u32 s38, s38, 0x1000
	s_addc_u32 s39, s39, 0
	s_add_u32 s40, s40, 0x1000
	s_addc_u32 s41, s41, 0
	s_add_u32 s42, s42, 0x1000
	s_addc_u32 s43, s43, 0
	s_add_u32 s44, s44, 0x1000
	s_addc_u32 s45, s45, 0
	s_add_u32 s46, s46, 0x1000
	s_addc_u32 s47, s47, 0
	s_add_u32 s48, s48, 0x1000
	s_addc_u32 s49, s49, 0
	s_add_u32 s60, s60, 0x1000
	s_addc_u32 s61, s61, 0
	s_add_u32 s62, s62, 0x1000
	s_addc_u32 s63, s63, 0
	global_load_dwordx4 v[64:67], v136, s[16:17] nt
	global_load_dwordx4 v[68:71], v136, s[18:19] nt
	global_load_dwordx4 v[72:75], v136, s[20:21] nt
	global_load_dwordx4 v[76:79], v136, s[22:23] nt
	global_load_dwordx4 v[80:83], v136, s[24:25] nt
	global_load_dwordx4 v[84:87], v136, s[26:27] nt
	global_load_dwordx4 v[88:91], v136, s[28:29] nt
	global_load_dwordx4 v[92:95], v136, s[30:31] nt
	global_load_dwordx4 v[96:99], v136, s[38:39] nt
	global_load_dwordx4 v[100:103], v136, s[40:41] nt
	global_load_dwordx4 v[104:107], v136, s[42:43] nt
	global_load_dwordx4 v[108:111], v136, s[44:45] nt
	global_load_dwordx4 v[112:115], v136, s[46:47] nt
	global_load_dwordx4 v[116:119], v136, s[48:49] nt
	global_load_dwordx4 v[120:123], v136, s[60:61] nt
	global_load_dwordx4 v[124:127], v136, s[62:63] nt
	s_waitcnt vmcnt(40)
; #define LAS __attribute__((address_space(3)))
; __device__ __forceinline__ unsigned pack4_fp8(float a, float b, float c, float d) { int r = 0; r = __builtin_amdgcn_cvt_pk_fp8_f32(a, b, r, false); r = __builtin_amdgcn_cvt_pk_fp8_f32(c, d, r, true); return (unsigned)r; }
; __device__ __forceinline__ void cvt8_to_lds(const f32x4 (&v)[16], LAS unsigned char* tile, int lane, int wv) {
; #pragma unroll
;     for (int i = 0; i < 4; ++i) { u32x4 w; w.x = pack4_fp8(v[0][i] * W8_SCALE, v[1][i] * W8_SCALE, v[2][i] * W8_SCALE, v[3][i] * W8_SCALE); w.y = pack4_fp8(v[4][i] * W8_SCALE, v[5][i] * W8_SCALE, v[6][i] * W8_SCALE, v[7][i] * W8_SCALE);
;         w.z = pack4_fp8(v[8][i] * W8_SCALE, v[9][i] * W8_SCALE, v[10][i] * W8_SCALE, v[11][i] * W8_SCALE); w.w = pack4_fp8(v[12][i] * W8_SCALE, v[13][i] * W8_SCALE, v[14][i] * W8_SCALE, v[15][i] * W8_SCALE);
;         *(LAS u32x4*)(tile + (4 * lane + i) * 128 + ((wv ^ (lane & 7)) << 4)) = w; }
; }
; __device__ __forceinline__ void cvt8_from_lds(const LAS unsigned char* tile, fp8_t* d, int ld_dst, int tid) {
;     const int c = tid & 7;
; #pragma unroll
;     for (int q = 0; q < 4; ++q) { const int r = (tid >> 3) + 64 * q; const u32x4 w = *(const LAS u32x4*)(tile + r * 128 + ((c ^ ((r >> 2) & 7)) << 4));
;         __builtin_nontemporal_store(w, (u32x4*)(d + (size_t)r * ld_dst + 16 * c)); }
; }
; __device__ __forceinline__ void cvt_item_lds(const float* src, int ld_src, fp8_t* dst, int ld_dst, LAS unsigned char* lds, int tid, int wv) {
;     const int lane = tid & 63;
;     const float* s = src + (size_t)(16 * wv) * ld_src + 4 * lane;
;     f32x4 va[16], vb[16];
;     cvt8_load(va, s, ld_src);
; #pragma unroll
;     for (int t = 0; t < 8; t += 2) {
;         cvt8_load(vb, s + (t + 1) * 256, ld_src); __builtin_amdgcn_sched_barrier(0);
;         cvt8_to_lds(va, lds, lane, wv); CVT_LDS_BAR(); __builtin_amdgcn_sched_barrier(0);
;         cvt8_from_lds(lds, dst + (size_t)(t * 256) * ld_dst, ld_dst, tid); __builtin_amdgcn_sched_barrier(0);
;         if (t + 2 < 8) { cvt8_load(va, s + (t + 2) * 256, ld_src); __builtin_amdgcn_sched_barrier(0); }
;         cvt8_to_lds(vb, lds + 32768, lane, wv); CVT_LDS_BAR(); __builtin_amdgcn_sched_barrier(0);
;         cvt8_from_lds(lds + 32768, dst + (size_t)((t + 1) * 256) * ld_dst, ld_dst, tid); __builtin_amdgcn_sched_barrier(0);
;     }
	v_mul_f32_e32 v128, 0x42800000, v128
	v_mul_f32_e32 v132, 0x42800000, v132
	v_mul_f32_e32 v148, 0x42800000, v148
	v_mul_f32_e32 v152, 0x42800000, v152
	v_mul_f32_e32 v156, 0x42800000, v156
	v_mul_f32_e32 v160, 0x42800000, v160
	v_mul_f32_e32 v164, 0x42800000, v164
	v_mul_f32_e32 v168, 0x42800000, v168
	v_mul_f32_e32 v172, 0x42800000, v172
	v_mul_f32_e32 v176, 0x42800000, v176
	v_mul_f32_e32 v180, 0x42800000, v180
	v_mul_f32_e32 v184, 0x42800000, v184
	v_mul_f32_e32 v188, 0x42800000, v188
	v_mul_f32_e32 v192, 0x42800000, v192
	v_mul_f32_e32 v196, 0x42800000, v196
	v_mul_f32_e32 v200, 0x42800000, v200
	v_cvt_pk_fp8_f32 v210, v128, v132
	v_cvt_pk_fp8_f32 v211, v156, v160
	v_cvt_pk_fp8_f32 v212, v172, v176
	v_cvt_pk_fp8_f32 v213, v188, v192
	v_cvt_pk_fp8_f32 v210, v148, v152 op_sel:[0,0,1]
	v_cvt_pk_fp8_f32 v211, v164, v168 op_sel:[0,0,1]
	v_cvt_pk_fp8_f32 v212, v180, v184 op_sel:[0,0,1]
	v_cvt_pk_fp8_f32 v213, v196, v200 op_sel:[0,0,1]
	ds_write_b128 v205, v[210:213] offset:0
	v_mul_f32_e32 v129, 0x42800000, v129
	v_mul_f32_e32 v133, 0x42800000, v133
	v_mul_f32_e32 v149, 0x42800000, v149
	v_mul_f32_e32 v153, 0x42800000, v153
	v_mul_f32_e32 v157, 0x42800000, v157
	v_mul_f32_e32 v161, 0x42800000, v161
	v_mul_f32_e32 v165, 0x42800000, v165
	v_mul_f32_e32 v169, 0x42800000, v169
	v_mul_f32_e32 v173, 0x42800000, v173
	v_mul_f32_e32 v177, 0x42800000, v177
	v_mul_f32_e32 v181, 0x42800000, v181
	v_mul_f32_e32 v185, 0x42800000, v185
	v_mul_f32_e32 v189, 0x42800000, v189
	v_mul_f32_e32 v193, 0x42800000, v193
	v_mul_f32_e32 v197, 0x42800000, v197
	v_mul_f32_e32 v201, 0x42800000, v201
	v_cvt_pk_fp8_f32 v210, v129, v133
	v_cvt_pk_fp8_f32 v211, v157, v161
	v_cvt_pk_fp8_f32 v212, v173, v177
	v_cvt_pk_fp8_f32 v213, v189, v193
	v_cvt_pk_fp8_f32 v210, v149, v153 op_sel:[0,0,1]
	v_cvt_pk_fp8_f32 v211, v165, v169 op_sel:[0,0,1]
	v_cvt_pk_fp8_f32 v212, v181, v185 op_sel:[0,0,1]
	v_cvt_pk_fp8_f32 v213, v197, v201 op_sel:[0,0,1]
	ds_write_b128 v205, v[210:213] offset:128
	v_mul_f32_e32 v130, 0x42800000, v130
	v_mul_f32_e32 v134, 0x42800000, v134
	v_mul_f32_e32 v150, 0x42800000, v150
	v_mul_f32_e32 v154, 0x42800000, v154
	v_mul_f32_e32 v158, 0x42800000, v158
	v_mul_f32_e32 v162, 0x42800000, v162
	v_mul_f32_e32 v166, 0x42800000, v166
	v_mul_f32_e32 v170, 0x42800000, v170
	v_mul_f32_e32 v174, 0x42800000, v174
	v_mul_f32_e32 v178, 0x42800000, v178
	v_mul_f32_e32 v182, 0x42800000, v182
	v_mul_f32_e32 v186, 0x42800000, v186
	v_mul_f32_e32 v190, 0x42800000, v190
	v_mul_f32_e32 v194, 0x42800000, v194
	v_mul_f32_e32 v198, 0x42800000, v198
	v_mul_f32_e32 v202, 0x42800000, v202
	v_cvt_pk_fp8_f32 v210, v130, v134
	v_cvt_pk_fp8_f32 v211, v158, v162
	v_cvt_pk_fp8_f32 v212, v174, v178
	v_cvt_pk_fp8_f32 v213, v190, v194
	v_cvt_pk_fp8_f32 v210, v150, v154 op_sel:[0,0,1]
	v_cvt_pk_fp8_f32 v211, v166, v170 op_sel:[0,0,1]
	v_cvt_pk_fp8_f32 v212, v182, v186 op_sel:[0,0,1]
	v_cvt_pk_fp8_f32 v213, v198, v202 op_sel:[0,0,1]
	ds_write_b128 v205, v[210:213] offset:256
	v_mul_f32_e32 v131, 0x42800000, v131
	v_mul_f32_e32 v135, 0x42800000, v135
	v_mul_f32_e32 v151, 0x42800000, v151
	v_mul_f32_e32 v155, 0x42800000, v155
	v_mul_f32_e32 v159, 0x42800000, v159
	v_mul_f32_e32 v163, 0x42800000, v163
	v_mul_f32_e32 v167, 0x42800000, v167
	v_mul_f32_e32 v171, 0x42800000, v171
	v_mul_f32_e32 v175, 0x42800000, v175
	v_mul_f32_e32 v179, 0x42800000, v179
	v_mul_f32_e32 v183, 0x42800000, v183
	v_mul_f32_e32 v187, 0x42800000, v187
	v_mul_f32_e32 v191, 0x42800000, v191
	v_mul_f32_e32 v195, 0x42800000, v195
	v_mul_f32_e32 v199, 0x42800000, v199
	v_mul_f32_e32 v203, 0x42800000, v203
	v_cvt_pk_fp8_f32 v210, v131, v135
	v_cvt_pk_fp8_f32 v211, v159, v163
	v_cvt_pk_fp8_f32 v212, v175, v179
	v_cvt_pk_fp8_f32 v213, v191, v195
	v_cvt_pk_fp8_f32 v210, v151, v155 op_sel:[0,0,1]
	v_cvt_pk_fp8_f32 v211, v167, v171 op_sel:[0,0,1]
	v_cvt_pk_fp8_f32 v212, v183, v187 op_sel:[0,0,1]
	v_cvt_pk_fp8_f32 v213, v199, v203 op_sel:[0,0,1]
	ds_write_b128 v205, v[210:213] offset:384
	s_waitcnt lgkmcnt(0)
	s_barrier
	ds_read_b128 v[128:131], v206
	ds_read_b128 v[132:135], v207
	ds_read_b128 v[148:151], v208
	ds_read_b128 v[152:155], v209
	v_add_u32_e32 v156, v140, v138
	v_add_u32_e32 v157, v142, v138
	v_add_u32_e32 v158, v144, v138
	v_add_u32_e32 v159, v146, v138
	s_waitcnt lgkmcnt(3)
	global_store_dwordx4 v156, v[128:131], s[64:65] nt
	s_waitcnt lgkmcnt(2)
	global_store_dwordx4 v157, v[132:135], s[64:65] nt
	s_waitcnt lgkmcnt(1)
	global_store_dwordx4 v158, v[148:151], s[64:65] nt
	s_waitcnt lgkmcnt(0)
	global_store_dwordx4 v159, v[152:155], s[64:65] nt
	s_add_u32 s64, s64, 0x80000
	s_addc_u32 s65, s65, 0
	s_nop 1
	global_load_dwordx4 v[128:131], v136, s[16:17] offset:1024 nt
	global_load_dwordx4 v[132:135], v136, s[18:19] offset:1024 nt
	global_load_dwordx4 v[148:151], v136, s[20:21] offset:1024 nt
	global_load_dwordx4 v[152:155], v136, s[22:23] offset:1024 nt
	global_load_dwordx4 v[156:159], v136, s[24:25] offset:1024 nt
	global_load_dwordx4 v[160:163], v136, s[26:27] offset:1024 nt
	global_load_dwordx4 v[164:167], v136, s[28:29] offset:1024 nt
	global_load_dwordx4 v[168:171], v136, s[30:31] offset:1024 nt
	global_load_dwordx4 v[172:175], v136, s[38:39] offset:1024 nt
	global_load_dwordx4 v[176:179], v136, s[40:41] offset:1024 nt
	global_load_dwordx4 v[180:183], v136, s[42:43] offset:1024 nt
	global_load_dwordx4 v[184:187], v136, s[44:45] offset:1024 nt
	global_load_dwordx4 v[188:191], v136, s[46:47] offset:1024 nt
	global_load_dwordx4 v[192:195], v136, s[48:49] offset:1024 nt
	global_load_dwordx4 v[196:199], v136, s[60:61] offset:1024 nt
	global_load_dwordx4 v[200:203], v136, s[62:63] offset:1024 nt
	s_waitcnt vmcnt(40)
; #define LAS __attribute__((address_space(3)))
; __device__ __forceinline__ unsigned pack4_fp8(float a, float b, float c, float d) { int r = 0; r = __builtin_amdgcn_cvt_pk_fp8_f32(a, b, r, false); r = __builtin_amdgcn_cvt_pk_fp8_f32(c, d, r, true); return (unsigned)r; }
; __device__ __forceinline__ void cvt8_to_lds(const f32x4 (&v)[16], LAS unsigned char* tile, int lane, int wv) {
; #pragma unroll
;     for (int i = 0; i < 4; ++i) { u32x4 w; w.x = pack4_fp8(v[0][i] * W8_SCALE, v[1][i] * W8_SCALE, v[2][i] * W8_SCALE, v[3][i] * W8_SCALE); w.y = pack4_fp8(v[4][i] * W8_SCALE, v[5][i] * W8_SCALE, v[6][i] * W8_SCALE, v[7][i] * W8_SCALE);
;         w.z = pack4_fp8(v[8][i] * W8_SCALE, v[9][i] * W8_SCALE, v[10][i] * W8_SCALE, v[11][i] * W8_SCALE); w.w = pack4_fp8(v[12][i] * W8_SCALE, v[13][i] * W8_SCALE, v[14][i] * W8_SCALE, v[15][i] * W8_SCALE);
;         *(LAS u32x4*)(tile + (4 * lane + i) * 128 + ((wv ^ (lane & 7)) << 4)) = w; }
; }
; __device__ __forceinline__ void cvt8_from_lds(const LAS unsigned char* tile, fp8_t* d, int ld_dst, int tid) {
;     const int c = tid & 7;
; #pragma unroll
;     for (int q = 0; q < 4; ++q) { const int r = (tid >> 3) + 64 * q; const u32x4 w = *(const LAS u32x4*)(tile + r * 128 + ((c ^ ((r >> 2) & 7)) << 4));
;         __builtin_nontemporal_store(w, (u32x4*)(d + (size_t)r * ld_dst + 16 * c)); }
; }
; __device__ __forceinline__ void cvt_item_lds(const float* src, int ld_src, fp8_t* dst, int ld_dst, LAS unsigned char* lds, int tid, int wv) {
;     const int lane = tid & 63;
;     const float* s = src + (size_t)(16 * wv) * ld_src + 4 * lane;
;     f32x4 va[16], vb[16];
;     cvt8_load(va, s, ld_src);
; #pragma unroll
;     for (int t = 0; t < 8; t += 2) {
;         cvt8_load(vb, s + (t + 1) * 256, ld_src); __builtin_amdgcn_sched_barrier(0);
;         cvt8_to_lds(va, lds, lane, wv); CVT_LDS_BAR(); __builtin_amdgcn_sched_barrier(0);
;         cvt8_from_lds(lds, dst + (size_t)(t * 256) * ld_dst, ld_dst, tid); __builtin_amdgcn_sched_barrier(0);
;         if (t + 2 < 8) { cvt8_load(va, s + (t + 2) * 256, ld_src); __builtin_amdgcn_sched_barrier(0); }
;         cvt8_to_lds(vb, lds + 32768, lane, wv); CVT_LDS_BAR(); __builtin_amdgcn_sched_barrier(0);
;         cvt8_from_lds(lds + 32768, dst + (size_t)((t + 1) * 256) * ld_dst, ld_dst, tid); __builtin_amdgcn_sched_barrier(0);
	v_mul_f32_e32 v0, 0x42800000, v0
	v_mul_f32_e32 v4, 0x42800000, v4
	v_mul_f32_e32 v8, 0x42800000, v8
	v_mul_f32_e32 v12, 0x42800000, v12
	v_mul_f32_e32 v16, 0x42800000, v16
	v_mul_f32_e32 v20, 0x42800000, v20
	v_mul_f32_e32 v24, 0x42800000, v24
	v_mul_f32_e32 v28, 0x42800000, v28
	v_mul_f32_e32 v32, 0x42800000, v32
	v_mul_f32_e32 v36, 0x42800000, v36
	v_mul_f32_e32 v40, 0x42800000, v40
	v_mul_f32_e32 v44, 0x42800000, v44
	v_mul_f32_e32 v48, 0x42800000, v48
	v_mul_f32_e32 v52, 0x42800000, v52
	v_mul_f32_e32 v56, 0x42800000, v56
	v_mul_f32_e32 v60, 0x42800000, v60
	v_cvt_pk_fp8_f32 v210, v0, v4
	v_cvt_pk_fp8_f32 v211, v16, v20
	v_cvt_pk_fp8_f32 v212, v32, v36
	v_cvt_pk_fp8_f32 v213, v48, v52
	v_cvt_pk_fp8_f32 v210, v8, v12 op_sel:[0,0,1]
	v_cvt_pk_fp8_f32 v211, v24, v28 op_sel:[0,0,1]
	v_cvt_pk_fp8_f32 v212, v40, v44 op_sel:[0,0,1]
	v_cvt_pk_fp8_f32 v213, v56, v60 op_sel:[0,0,1]
	ds_write_b128 v205, v[210:213] offset:32768
	v_mul_f32_e32 v1, 0x42800000, v1
	v_mul_f32_e32 v5, 0x42800000, v5
	v_mul_f32_e32 v9, 0x42800000, v9
	v_mul_f32_e32 v13, 0x42800000, v13
	v_mul_f32_e32 v17, 0x42800000, v17
	v_mul_f32_e32 v21, 0x42800000, v21
	v_mul_f32_e32 v25, 0x42800000, v25
	v_mul_f32_e32 v29, 0x42800000, v29
	v_mul_f32_e32 v33, 0x42800000, v33
	v_mul_f32_e32 v37, 0x42800000, v37
	v_mul_f32_e32 v41, 0x42800000, v41
	v_mul_f32_e32 v45, 0x42800000, v45
	v_mul_f32_e32 v49, 0x42800000, v49
	v_mul_f32_e32 v53, 0x42800000, v53
	v_mul_f32_e32 v57, 0x42800000, v57
	v_mul_f32_e32 v61, 0x42800000, v61
	v_cvt_pk_fp8_f32 v210, v1, v5
	v_cvt_pk_fp8_f32 v211, v17, v21
	v_cvt_pk_fp8_f32 v212, v33, v37
	v_cvt_pk_fp8_f32 v213, v49, v53
	v_cvt_pk_fp8_f32 v210, v9, v13 op_sel:[0,0,1]
	v_cvt_pk_fp8_f32 v211, v25, v29 op_sel:[0,0,1]
	v_cvt_pk_fp8_f32 v212, v41, v45 op_sel:[0,0,1]
	v_cvt_pk_fp8_f32 v213, v57, v61 op_sel:[0,0,1]
	ds_write_b128 v205, v[210:213] offset:32896
	v_mul_f32_e32 v2, 0x42800000, v2
	v_mul_f32_e32 v6, 0x42800000, v6
	v_mul_f32_e32 v10, 0x42800000, v10
	v_mul_f32_e32 v14, 0x42800000, v14
	v_mul_f32_e32 v18, 0x42800000, v18
	v_mul_f32_e32 v22, 0x42800000, v22
	v_mul_f32_e32 v26, 0x42800000, v26
	v_mul_f32_e32 v30, 0x42800000, v30
	v_mul_f32_e32 v34, 0x42800000, v34
	v_mul_f32_e32 v38, 0x42800000, v38
	v_mul_f32_e32 v42, 0x42800000, v42
	v_mul_f32_e32 v46, 0x42800000, v46
	v_mul_f32_e32 v50, 0x42800000, v50
	v_mul_f32_e32 v54, 0x42800000, v54
	v_mul_f32_e32 v58, 0x42800000, v58
	v_mul_f32_e32 v62, 0x42800000, v62
	v_cvt_pk_fp8_f32 v210, v2, v6
	v_cvt_pk_fp8_f32 v211, v18, v22
	v_cvt_pk_fp8_f32 v212, v34, v38
	v_cvt_pk_fp8_f32 v213, v50, v54
	v_cvt_pk_fp8_f32 v210, v10, v14 op_sel:[0,0,1]
	v_cvt_pk_fp8_f32 v211, v26, v30 op_sel:[0,0,1]
	v_cvt_pk_fp8_f32 v212, v42, v46 op_sel:[0,0,1]
	v_cvt_pk_fp8_f32 v213, v58, v62 op_sel:[0,0,1]
	ds_write_b128 v205, v[210:213] offset:33024
	v_mul_f32_e32 v3, 0x42800000, v3
	v_mul_f32_e32 v7, 0x42800000, v7
	v_mul_f32_e32 v11, 0x42800000, v11
	v_mul_f32_e32 v15, 0x42800000, v15
	v_mul_f32_e32 v19, 0x42800000, v19
	v_mul_f32_e32 v23, 0x42800000, v23
	v_mul_f32_e32 v27, 0x42800000, v27
	v_mul_f32_e32 v31, 0x42800000, v31
	v_mul_f32_e32 v35, 0x42800000, v35
	v_mul_f32_e32 v39, 0x42800000, v39
	v_mul_f32_e32 v43, 0x42800000, v43
	v_mul_f32_e32 v47, 0x42800000, v47
	v_mul_f32_e32 v51, 0x42800000, v51
	v_mul_f32_e32 v55, 0x42800000, v55
	v_mul_f32_e32 v59, 0x42800000, v59
	v_mul_f32_e32 v63, 0x42800000, v63
	v_cvt_pk_fp8_f32 v210, v3, v7
	v_cvt_pk_fp8_f32 v211, v19, v23
	v_cvt_pk_fp8_f32 v212, v35, v39
	v_cvt_pk_fp8_f32 v213, v51, v55
	v_cvt_pk_fp8_f32 v210, v11, v15 op_sel:[0,0,1]
	v_cvt_pk_fp8_f32 v211, v27, v31 op_sel:[0,0,1]
	v_cvt_pk_fp8_f32 v212, v43, v47 op_sel:[0,0,1]
	v_cvt_pk_fp8_f32 v213, v59, v63 op_sel:[0,0,1]
	ds_write_b128 v205, v[210:213] offset:33152
	s_waitcnt lgkmcnt(0)
	s_barrier
	ds_read_b128 v[0:3], v206 offset:32768
	ds_read_b128 v[4:7], v207 offset:32768
	ds_read_b128 v[8:11], v208 offset:32768
	ds_read_b128 v[12:15], v209 offset:32768
	v_add_u32_e32 v16, v140, v138
	v_add_u32_e32 v17, v142, v138
	v_add_u32_e32 v18, v144, v138
	v_add_u32_e32 v19, v146, v138
	s_waitcnt lgkmcnt(3)
	global_store_dwordx4 v16, v[0:3], s[64:65] nt
	s_waitcnt lgkmcnt(2)
	global_store_dwordx4 v17, v[4:7], s[64:65] nt
	s_waitcnt lgkmcnt(1)
	global_store_dwordx4 v18, v[8:11], s[64:65] nt
	s_waitcnt lgkmcnt(0)
	global_store_dwordx4 v19, v[12:15], s[64:65] nt
	s_add_u32 s64, s64, 0x80000
	s_addc_u32 s65, s65, 0
	s_nop 1
	global_load_dwordx4 v[0:3], v136, s[16:17] offset:2048 nt
	global_load_dwordx4 v[4:7], v136, s[18:19] offset:2048 nt
	global_load_dwordx4 v[8:11], v136, s[20:21] offset:2048 nt
	global_load_dwordx4 v[12:15], v136, s[22:23] offset:2048 nt
	global_load_dwordx4 v[16:19], v136, s[24:25] offset:2048 nt
	global_load_dwordx4 v[20:23], v136, s[26:27] offset:2048 nt
	global_load_dwordx4 v[24:27], v136, s[28:29] offset:2048 nt
	global_load_dwordx4 v[28:31], v136, s[30:31] offset:2048 nt
	global_load_dwordx4 v[32:35], v136, s[38:39] offset:2048 nt
	global_load_dwordx4 v[36:39], v136, s[40:41] offset:2048 nt
	global_load_dwordx4 v[40:43], v136, s[42:43] offset:2048 nt
	global_load_dwordx4 v[44:47], v136, s[44:45] offset:2048 nt
	global_load_dwordx4 v[48:51], v136, s[46:47] offset:2048 nt
	global_load_dwordx4 v[52:55], v136, s[48:49] offset:2048 nt
	global_load_dwordx4 v[56:59], v136, s[60:61] offset:2048 nt
	global_load_dwordx4 v[60:63], v136, s[62:63] offset:2048 nt
	s_waitcnt vmcnt(40)
; #define LAS __attribute__((address_space(3)))
; __device__ __forceinline__ unsigned pack4_fp8(float a, float b, float c, float d) { int r = 0; r = __builtin_amdgcn_cvt_pk_fp8_f32(a, b, r, false); r = __builtin_amdgcn_cvt_pk_fp8_f32(c, d, r, true); return (unsigned)r; }
; __device__ __forceinline__ void cvt8_to_lds(const f32x4 (&v)[16], LAS unsigned char* tile, int lane, int wv) {
; #pragma unroll
;     for (int i = 0; i < 4; ++i) { u32x4 w; w.x = pack4_fp8(v[0][i] * W8_SCALE, v[1][i] * W8_SCALE, v[2][i] * W8_SCALE, v[3][i] * W8_SCALE); w.y = pack4_fp8(v[4][i] * W8_SCALE, v[5][i] * W8_SCALE, v[6][i] * W8_SCALE, v[7][i] * W8_SCALE);
;         w.z = pack4_fp8(v[8][i] * W8_SCALE, v[9][i] * W8_SCALE, v[10][i] * W8_SCALE, v[11][i] * W8_SCALE); w.w = pack4_fp8(v[12][i] * W8_SCALE, v[13][i] * W8_SCALE, v[14][i] * W8_SCALE, v[15][i] * W8_SCALE);
;         *(LAS u32x4*)(tile + (4 * lane + i) * 128 + ((wv ^ (lane & 7)) << 4)) = w; }
; }
; __device__ __forceinline__ void cvt8_from_lds(const LAS unsigned char* tile, fp8_t* d, int ld_dst, int tid) {
;     const int c = tid & 7;
; #pragma unroll
;     for (int q = 0; q < 4; ++q) { const int r = (tid >> 3) + 64 * q; const u32x4 w = *(const LAS u32x4*)(tile + r * 128 + ((c ^ ((r >> 2) & 7)) << 4));
;         __builtin_nontemporal_store(w, (u32x4*)(d + (size_t)r * ld_dst + 16 * c)); }
; }
; __device__ __forceinline__ void cvt_item_lds(const float* src, int ld_src, fp8_t* dst, int ld_dst, LAS unsigned char* lds, int tid, int wv) {
;     const int lane = tid & 63;
;     const float* s = src + (size_t)(16 * wv) * ld_src + 4 * lane;
;     f32x4 va[16], vb[16];
;     cvt8_load(va, s, ld_src);
; #pragma unroll
;     for (int t = 0; t < 8; t += 2) {
;         cvt8_load(vb, s + (t + 1) * 256, ld_src); __builtin_amdgcn_sched_barrier(0);
;         cvt8_to_lds(va, lds, lane, wv); CVT_LDS_BAR(); __builtin_amdgcn_sched_barrier(0);
;         cvt8_from_lds(lds, dst + (size_t)(t * 256) * ld_dst, ld_dst, tid); __builtin_amdgcn_sched_barrier(0);
;         if (t + 2 < 8) { cvt8_load(va, s + (t + 2) * 256, ld_src); __builtin_amdgcn_sched_barrier(0); }
;         cvt8_to_lds(vb, lds + 32768, lane, wv); CVT_LDS_BAR(); __builtin_amdgcn_sched_barrier(0);
;         cvt8_from_lds(lds + 32768, dst + (size_t)((t + 1) * 256) * ld_dst, ld_dst, tid); __builtin_amdgcn_sched_barrier(0);
	v_mul_f32_e32 v64, 0x42800000, v64
	v_mul_f32_e32 v68, 0x42800000, v68
	v_mul_f32_e32 v72, 0x42800000, v72
	v_mul_f32_e32 v76, 0x42800000, v76
	v_mul_f32_e32 v80, 0x42800000, v80
	v_mul_f32_e32 v84, 0x42800000, v84
	v_mul_f32_e32 v88, 0x42800000, v88
	v_mul_f32_e32 v92, 0x42800000, v92
	v_mul_f32_e32 v96, 0x42800000, v96
	v_mul_f32_e32 v100, 0x42800000, v100
	v_mul_f32_e32 v104, 0x42800000, v104
	v_mul_f32_e32 v108, 0x42800000, v108
	v_mul_f32_e32 v112, 0x42800000, v112
	v_mul_f32_e32 v116, 0x42800000, v116
	v_mul_f32_e32 v120, 0x42800000, v120
	v_mul_f32_e32 v124, 0x42800000, v124
	v_cvt_pk_fp8_f32 v210, v64, v68
	v_cvt_pk_fp8_f32 v211, v80, v84
	v_cvt_pk_fp8_f32 v212, v96, v100
	v_cvt_pk_fp8_f32 v213, v112, v116
	v_cvt_pk_fp8_f32 v210, v72, v76 op_sel:[0,0,1]
	v_cvt_pk_fp8_f32 v211, v88, v92 op_sel:[0,0,1]
	v_cvt_pk_fp8_f32 v212, v104, v108 op_sel:[0,0,1]
	v_cvt_pk_fp8_f32 v213, v120, v124 op_sel:[0,0,1]
	ds_write_b128 v205, v[210:213] offset:0
	v_mul_f32_e32 v65, 0x42800000, v65
	v_mul_f32_e32 v69, 0x42800000, v69
	v_mul_f32_e32 v73, 0x42800000, v73
	v_mul_f32_e32 v77, 0x42800000, v77
	v_mul_f32_e32 v81, 0x42800000, v81
	v_mul_f32_e32 v85, 0x42800000, v85
	v_mul_f32_e32 v89, 0x42800000, v89
	v_mul_f32_e32 v93, 0x42800000, v93
	v_mul_f32_e32 v97, 0x42800000, v97
	v_mul_f32_e32 v101, 0x42800000, v101
	v_mul_f32_e32 v105, 0x42800000, v105
	v_mul_f32_e32 v109, 0x42800000, v109
	v_mul_f32_e32 v113, 0x42800000, v113
	v_mul_f32_e32 v117, 0x42800000, v117
	v_mul_f32_e32 v121, 0x42800000, v121
	v_mul_f32_e32 v125, 0x42800000, v125
	v_cvt_pk_fp8_f32 v210, v65, v69
	v_cvt_pk_fp8_f32 v211, v81, v85
	v_cvt_pk_fp8_f32 v212, v97, v101
	v_cvt_pk_fp8_f32 v213, v113, v117
	v_cvt_pk_fp8_f32 v210, v73, v77 op_sel:[0,0,1]
	v_cvt_pk_fp8_f32 v211, v89, v93 op_sel:[0,0,1]
	v_cvt_pk_fp8_f32 v212, v105, v109 op_sel:[0,0,1]
	v_cvt_pk_fp8_f32 v213, v121, v125 op_sel:[0,0,1]
	ds_write_b128 v205, v[210:213] offset:128
	v_mul_f32_e32 v66, 0x42800000, v66
	v_mul_f32_e32 v70, 0x42800000, v70
	v_mul_f32_e32 v74, 0x42800000, v74
	v_mul_f32_e32 v78, 0x42800000, v78
	v_mul_f32_e32 v82, 0x42800000, v82
	v_mul_f32_e32 v86, 0x42800000, v86
	v_mul_f32_e32 v90, 0x42800000, v90
	v_mul_f32_e32 v94, 0x42800000, v94
	v_mul_f32_e32 v98, 0x42800000, v98
	v_mul_f32_e32 v102, 0x42800000, v102
	v_mul_f32_e32 v106, 0x42800000, v106
	v_mul_f32_e32 v110, 0x42800000, v110
	v_mul_f32_e32 v114, 0x42800000, v114
	v_mul_f32_e32 v118, 0x42800000, v118
	v_mul_f32_e32 v122, 0x42800000, v122
	v_mul_f32_e32 v126, 0x42800000, v126
	v_cvt_pk_fp8_f32 v210, v66, v70
	v_cvt_pk_fp8_f32 v211, v82, v86
	v_cvt_pk_fp8_f32 v212, v98, v102
	v_cvt_pk_fp8_f32 v213, v114, v118
	v_cvt_pk_fp8_f32 v210, v74, v78 op_sel:[0,0,1]
	v_cvt_pk_fp8_f32 v211, v90, v94 op_sel:[0,0,1]
	v_cvt_pk_fp8_f32 v212, v106, v110 op_sel:[0,0,1]
	v_cvt_pk_fp8_f32 v213, v122, v126 op_sel:[0,0,1]
	ds_write_b128 v205, v[210:213] offset:256
	v_mul_f32_e32 v67, 0x42800000, v67
	v_mul_f32_e32 v71, 0x42800000, v71
	v_mul_f32_e32 v75, 0x42800000, v75
	v_mul_f32_e32 v79, 0x42800000, v79
	v_mul_f32_e32 v83, 0x42800000, v83
	v_mul_f32_e32 v87, 0x42800000, v87
	v_mul_f32_e32 v91, 0x42800000, v91
	v_mul_f32_e32 v95, 0x42800000, v95
	v_mul_f32_e32 v99, 0x42800000, v99
	v_mul_f32_e32 v103, 0x42800000, v103
	v_mul_f32_e32 v107, 0x42800000, v107
	v_mul_f32_e32 v111, 0x42800000, v111
	v_mul_f32_e32 v115, 0x42800000, v115
	v_mul_f32_e32 v119, 0x42800000, v119
	v_mul_f32_e32 v123, 0x42800000, v123
	v_mul_f32_e32 v127, 0x42800000, v127
	v_cvt_pk_fp8_f32 v210, v67, v71
	v_cvt_pk_fp8_f32 v211, v83, v87
	v_cvt_pk_fp8_f32 v212, v99, v103
	v_cvt_pk_fp8_f32 v213, v115, v119
	v_cvt_pk_fp8_f32 v210, v75, v79 op_sel:[0,0,1]
	v_cvt_pk_fp8_f32 v211, v91, v95 op_sel:[0,0,1]
	v_cvt_pk_fp8_f32 v212, v107, v111 op_sel:[0,0,1]
	v_cvt_pk_fp8_f32 v213, v123, v127 op_sel:[0,0,1]
	ds_write_b128 v205, v[210:213] offset:384
	s_waitcnt lgkmcnt(0)
	s_barrier
	ds_read_b128 v[64:67], v206
	ds_read_b128 v[68:71], v207
	ds_read_b128 v[72:75], v208
	ds_read_b128 v[76:79], v209
	v_add_u32_e32 v80, v140, v138
	v_add_u32_e32 v81, v142, v138
	v_add_u32_e32 v82, v144, v138
	v_add_u32_e32 v83, v146, v138
	s_waitcnt lgkmcnt(3)
	global_store_dwordx4 v80, v[64:67], s[64:65] nt
	s_waitcnt lgkmcnt(2)
	global_store_dwordx4 v81, v[68:71], s[64:65] nt
	s_waitcnt lgkmcnt(1)
	global_store_dwordx4 v82, v[72:75], s[64:65] nt
	s_waitcnt lgkmcnt(0)
	global_store_dwordx4 v83, v[76:79], s[64:65] nt
	s_add_u32 s64, s64, 0x80000
	s_addc_u32 s65, s65, 0
	s_nop 1
	global_load_dwordx4 v[64:67], v136, s[16:17] offset:3072 nt
	global_load_dwordx4 v[68:71], v136, s[18:19] offset:3072 nt
	global_load_dwordx4 v[72:75], v136, s[20:21] offset:3072 nt
	global_load_dwordx4 v[76:79], v136, s[22:23] offset:3072 nt
	global_load_dwordx4 v[80:83], v136, s[24:25] offset:3072 nt
	global_load_dwordx4 v[84:87], v136, s[26:27] offset:3072 nt
	global_load_dwordx4 v[88:91], v136, s[28:29] offset:3072 nt
	global_load_dwordx4 v[92:95], v136, s[30:31] offset:3072 nt
	global_load_dwordx4 v[96:99], v136, s[38:39] offset:3072 nt
	global_load_dwordx4 v[100:103], v136, s[40:41] offset:3072 nt
	global_load_dwordx4 v[104:107], v136, s[42:43] offset:3072 nt
	global_load_dwordx4 v[108:111], v136, s[44:45] offset:3072 nt
	global_load_dwordx4 v[112:115], v136, s[46:47] offset:3072 nt
	global_load_dwordx4 v[116:119], v136, s[48:49] offset:3072 nt
	global_load_dwordx4 v[120:123], v136, s[60:61] offset:3072 nt
	global_load_dwordx4 v[124:127], v136, s[62:63] offset:3072 nt
	s_waitcnt vmcnt(40)
; #define LAS __attribute__((address_space(3)))
; __device__ __forceinline__ unsigned pack4_fp8(float a, float b, float c, float d) { int r = 0; r = __builtin_amdgcn_cvt_pk_fp8_f32(a, b, r, false); r = __builtin_amdgcn_cvt_pk_fp8_f32(c, d, r, true); return (unsigned)r; }
; __device__ __forceinline__ void cvt8_to_lds(const f32x4 (&v)[16], LAS unsigned char* tile, int lane, int wv) {
; #pragma unroll
;     for (int i = 0; i < 4; ++i) { u32x4 w; w.x = pack4_fp8(v[0][i] * W8_SCALE, v[1][i] * W8_SCALE, v[2][i] * W8_SCALE, v[3][i] * W8_SCALE); w.y = pack4_fp8(v[4][i] * W8_SCALE, v[5][i] * W8_SCALE, v[6][i] * W8_SCALE, v[7][i] * W8_SCALE);
;         w.z = pack4_fp8(v[8][i] * W8_SCALE, v[9][i] * W8_SCALE, v[10][i] * W8_SCALE, v[11][i] * W8_SCALE); w.w = pack4_fp8(v[12][i] * W8_SCALE, v[13][i] * W8_SCALE, v[14][i] * W8_SCALE, v[15][i] * W8_SCALE);
;         *(LAS u32x4*)(tile + (4 * lane + i) * 128 + ((wv ^ (lane & 7)) << 4)) = w; }
; }
; __device__ __forceinline__ void cvt8_from_lds(const LAS unsigned char* tile, fp8_t* d, int ld_dst, int tid) {
;     const int c = tid & 7;
; #pragma unroll
;     for (int q = 0; q < 4; ++q) { const int r = (tid >> 3) + 64 * q; const u32x4 w = *(const LAS u32x4*)(tile + r * 128 + ((c ^ ((r >> 2) & 7)) << 4));
;         __builtin_nontemporal_store(w, (u32x4*)(d + (size_t)r * ld_dst + 16 * c)); }
; }
; __device__ __forceinline__ void cvt_item_lds(const float* src, int ld_src, fp8_t* dst, int ld_dst, LAS unsigned char* lds, int tid, int wv) {
;     const int lane = tid & 63;
;     const float* s = src + (size_t)(16 * wv) * ld_src + 4 * lane;
;     f32x4 va[16], vb[16];
;     cvt8_load(va, s, ld_src);
; #pragma unroll
;     for (int t = 0; t < 8; t += 2) {
;         cvt8_load(vb, s + (t + 1) * 256, ld_src); __builtin_amdgcn_sched_barrier(0);
;         cvt8_to_lds(va, lds, lane, wv); CVT_LDS_BAR(); __builtin_amdgcn_sched_barrier(0);
;         cvt8_from_lds(lds, dst + (size_t)(t * 256) * ld_dst, ld_dst, tid); __builtin_amdgcn_sched_barrier(0);
;         if (t + 2 < 8) { cvt8_load(va, s + (t + 2) * 256, ld_src); __builtin_amdgcn_sched_barrier(0); }
;         cvt8_to_lds(vb, lds + 32768, lane, wv); CVT_LDS_BAR(); __builtin_amdgcn_sched_barrier(0);
;         cvt8_from_lds(lds + 32768, dst + (size_t)((t + 1) * 256) * ld_dst, ld_dst, tid); __builtin_amdgcn_sched_barrier(0);
	v_mul_f32_e32 v128, 0x42800000, v128
	v_mul_f32_e32 v132, 0x42800000, v132
	v_mul_f32_e32 v148, 0x42800000, v148
	v_mul_f32_e32 v152, 0x42800000, v152
	v_mul_f32_e32 v156, 0x42800000, v156
	v_mul_f32_e32 v160, 0x42800000, v160
	v_mul_f32_e32 v164, 0x42800000, v164
	v_mul_f32_e32 v168, 0x42800000, v168
	v_mul_f32_e32 v172, 0x42800000, v172
	v_mul_f32_e32 v176, 0x42800000, v176
	v_mul_f32_e32 v180, 0x42800000, v180
	v_mul_f32_e32 v184, 0x42800000, v184
	v_mul_f32_e32 v188, 0x42800000, v188
	v_mul_f32_e32 v192, 0x42800000, v192
	v_mul_f32_e32 v196, 0x42800000, v196
	v_mul_f32_e32 v200, 0x42800000, v200
	v_cvt_pk_fp8_f32 v210, v128, v132
	v_cvt_pk_fp8_f32 v211, v156, v160
	v_cvt_pk_fp8_f32 v212, v172, v176
	v_cvt_pk_fp8_f32 v213, v188, v192
	v_cvt_pk_fp8_f32 v210, v148, v152 op_sel:[0,0,1]
	v_cvt_pk_fp8_f32 v211, v164, v168 op_sel:[0,0,1]
	v_cvt_pk_fp8_f32 v212, v180, v184 op_sel:[0,0,1]
	v_cvt_pk_fp8_f32 v213, v196, v200 op_sel:[0,0,1]
	ds_write_b128 v205, v[210:213] offset:32768
	v_mul_f32_e32 v129, 0x42800000, v129
	v_mul_f32_e32 v133, 0x42800000, v133
	v_mul_f32_e32 v149, 0x42800000, v149
	v_mul_f32_e32 v153, 0x42800000, v153
	v_mul_f32_e32 v157, 0x42800000, v157
	v_mul_f32_e32 v161, 0x42800000, v161
	v_mul_f32_e32 v165, 0x42800000, v165
	v_mul_f32_e32 v169, 0x42800000, v169
	v_mul_f32_e32 v173, 0x42800000, v173
	v_mul_f32_e32 v177, 0x42800000, v177
	v_mul_f32_e32 v181, 0x42800000, v181
	v_mul_f32_e32 v185, 0x42800000, v185
	v_mul_f32_e32 v189, 0x42800000, v189
	v_mul_f32_e32 v193, 0x42800000, v193
	v_mul_f32_e32 v197, 0x42800000, v197
	v_mul_f32_e32 v201, 0x42800000, v201
	v_cvt_pk_fp8_f32 v210, v129, v133
	v_cvt_pk_fp8_f32 v211, v157, v161
	v_cvt_pk_fp8_f32 v212, v173, v177
	v_cvt_pk_fp8_f32 v213, v189, v193
	v_cvt_pk_fp8_f32 v210, v149, v153 op_sel:[0,0,1]
	v_cvt_pk_fp8_f32 v211, v165, v169 op_sel:[0,0,1]
	v_cvt_pk_fp8_f32 v212, v181, v185 op_sel:[0,0,1]
	v_cvt_pk_fp8_f32 v213, v197, v201 op_sel:[0,0,1]
	ds_write_b128 v205, v[210:213] offset:32896
	v_mul_f32_e32 v130, 0x42800000, v130
	v_mul_f32_e32 v134, 0x42800000, v134
	v_mul_f32_e32 v150, 0x42800000, v150
	v_mul_f32_e32 v154, 0x42800000, v154
	v_mul_f32_e32 v158, 0x42800000, v158
	v_mul_f32_e32 v162, 0x42800000, v162
	v_mul_f32_e32 v166, 0x42800000, v166
	v_mul_f32_e32 v170, 0x42800000, v170
	v_mul_f32_e32 v174, 0x42800000, v174
	v_mul_f32_e32 v178, 0x42800000, v178
	v_mul_f32_e32 v182, 0x42800000, v182
	v_mul_f32_e32 v186, 0x42800000, v186
	v_mul_f32_e32 v190, 0x42800000, v190
	v_mul_f32_e32 v194, 0x42800000, v194
	v_mul_f32_e32 v198, 0x42800000, v198
	v_mul_f32_e32 v202, 0x42800000, v202
	v_cvt_pk_fp8_f32 v210, v130, v134
	v_cvt_pk_fp8_f32 v211, v158, v162
	v_cvt_pk_fp8_f32 v212, v174, v178
	v_cvt_pk_fp8_f32 v213, v190, v194
	v_cvt_pk_fp8_f32 v210, v150, v154 op_sel:[0,0,1]
	v_cvt_pk_fp8_f32 v211, v166, v170 op_sel:[0,0,1]
	v_cvt_pk_fp8_f32 v212, v182, v186 op_sel:[0,0,1]
	v_cvt_pk_fp8_f32 v213, v198, v202 op_sel:[0,0,1]
	ds_write_b128 v205, v[210:213] offset:33024
	v_mul_f32_e32 v131, 0x42800000, v131
	v_mul_f32_e32 v135, 0x42800000, v135
	v_mul_f32_e32 v151, 0x42800000, v151
	v_mul_f32_e32 v155, 0x42800000, v155
	v_mul_f32_e32 v159, 0x42800000, v159
	v_mul_f32_e32 v163, 0x42800000, v163
	v_mul_f32_e32 v167, 0x42800000, v167
	v_mul_f32_e32 v171, 0x42800000, v171
	v_mul_f32_e32 v175, 0x42800000, v175
	v_mul_f32_e32 v179, 0x42800000, v179
	v_mul_f32_e32 v183, 0x42800000, v183
	v_mul_f32_e32 v187, 0x42800000, v187
	v_mul_f32_e32 v191, 0x42800000, v191
	v_mul_f32_e32 v195, 0x42800000, v195
	v_mul_f32_e32 v199, 0x42800000, v199
	v_mul_f32_e32 v203, 0x42800000, v203
	v_cvt_pk_fp8_f32 v210, v131, v135
	v_cvt_pk_fp8_f32 v211, v159, v163
	v_cvt_pk_fp8_f32 v212, v175, v179
	v_cvt_pk_fp8_f32 v213, v191, v195
	v_cvt_pk_fp8_f32 v210, v151, v155 op_sel:[0,0,1]
	v_cvt_pk_fp8_f32 v211, v167, v171 op_sel:[0,0,1]
	v_cvt_pk_fp8_f32 v212, v183, v187 op_sel:[0,0,1]
	v_cvt_pk_fp8_f32 v213, v199, v203 op_sel:[0,0,1]
	ds_write_b128 v205, v[210:213] offset:33152
	s_waitcnt lgkmcnt(0)
	s_barrier
	ds_read_b128 v[128:131], v206 offset:32768
	ds_read_b128 v[132:135], v207 offset:32768
	ds_read_b128 v[148:151], v208 offset:32768
	ds_read_b128 v[152:155], v209 offset:32768
	v_add_u32_e32 v156, v140, v138
	v_add_u32_e32 v157, v142, v138
	v_add_u32_e32 v158, v144, v138
	v_add_u32_e32 v159, v146, v138
	s_waitcnt lgkmcnt(3)
	global_store_dwordx4 v156, v[128:131], s[64:65] nt
	s_waitcnt lgkmcnt(2)
	global_store_dwordx4 v157, v[132:135], s[64:65] nt
	s_waitcnt lgkmcnt(1)
	global_store_dwordx4 v158, v[148:151], s[64:65] nt
	s_waitcnt lgkmcnt(0)
	global_store_dwordx4 v159, v[152:155], s[64:65] nt
	s_add_u32 s64, s64, 0x80000
	s_addc_u32 s65, s65, 0
	s_waitcnt vmcnt(24)
; #define LAS __attribute__((address_space(3)))
; __device__ __forceinline__ unsigned pack4_fp8(float a, float b, float c, float d) { int r = 0; r = __builtin_amdgcn_cvt_pk_fp8_f32(a, b, r, false); r = __builtin_amdgcn_cvt_pk_fp8_f32(c, d, r, true); return (unsigned)r; }
; __device__ __forceinline__ void cvt8_to_lds(const f32x4 (&v)[16], LAS unsigned char* tile, int lane, int wv) {
; #pragma unroll
;     for (int i = 0; i < 4; ++i) { u32x4 w; w.x = pack4_fp8(v[0][i] * W8_SCALE, v[1][i] * W8_SCALE, v[2][i] * W8_SCALE, v[3][i] * W8_SCALE); w.y = pack4_fp8(v[4][i] * W8_SCALE, v[5][i] * W8_SCALE, v[6][i] * W8_SCALE, v[7][i] * W8_SCALE);
;         w.z = pack4_fp8(v[8][i] * W8_SCALE, v[9][i] * W8_SCALE, v[10][i] * W8_SCALE, v[11][i] * W8_SCALE); w.w = pack4_fp8(v[12][i] * W8_SCALE, v[13][i] * W8_SCALE, v[14][i] * W8_SCALE, v[15][i] * W8_SCALE);
;         *(LAS u32x4*)(tile + (4 * lane + i) * 128 + ((wv ^ (lane & 7)) << 4)) = w; }
; }
; __device__ __forceinline__ void cvt8_from_lds(const LAS unsigned char* tile, fp8_t* d, int ld_dst, int tid) {
;     const int c = tid & 7;
; #pragma unroll
;     for (int q = 0; q < 4; ++q) { const int r = (tid >> 3) + 64 * q; const u32x4 w = *(const LAS u32x4*)(tile + r * 128 + ((c ^ ((r >> 2) & 7)) << 4));
;         __builtin_nontemporal_store(w, (u32x4*)(d + (size_t)r * ld_dst + 16 * c)); }
; }
; __device__ __forceinline__ void cvt_item_lds(const float* src, int ld_src, fp8_t* dst, int ld_dst, LAS unsigned char* lds, int tid, int wv) {
;     const int lane = tid & 63;
;     const float* s = src + (size_t)(16 * wv) * ld_src + 4 * lane;
;     f32x4 va[16], vb[16];
;     cvt8_load(va, s, ld_src);
; #pragma unroll
;     for (int t = 0; t < 8; t += 2) {
;         cvt8_load(vb, s + (t + 1) * 256, ld_src); __builtin_amdgcn_sched_barrier(0);
;         cvt8_to_lds(va, lds, lane, wv); CVT_LDS_BAR(); __builtin_amdgcn_sched_barrier(0);
;         cvt8_from_lds(lds, dst + (size_t)(t * 256) * ld_dst, ld_dst, tid); __builtin_amdgcn_sched_barrier(0);
;         if (t + 2 < 8) { cvt8_load(va, s + (t + 2) * 256, ld_src); __builtin_amdgcn_sched_barrier(0); }
;         cvt8_to_lds(vb, lds + 32768, lane, wv); CVT_LDS_BAR(); __builtin_amdgcn_sched_barrier(0);
;         cvt8_from_lds(lds + 32768, dst + (size_t)((t + 1) * 256) * ld_dst, ld_dst, tid); __builtin_amdgcn_sched_barrier(0);
	v_mul_f32_e32 v0, 0x42800000, v0
	v_mul_f32_e32 v4, 0x42800000, v4
	v_mul_f32_e32 v8, 0x42800000, v8
	v_mul_f32_e32 v12, 0x42800000, v12
	v_mul_f32_e32 v16, 0x42800000, v16
	v_mul_f32_e32 v20, 0x42800000, v20
	v_mul_f32_e32 v24, 0x42800000, v24
	v_mul_f32_e32 v28, 0x42800000, v28
	v_mul_f32_e32 v32, 0x42800000, v32
	v_mul_f32_e32 v36, 0x42800000, v36
	v_mul_f32_e32 v40, 0x42800000, v40
	v_mul_f32_e32 v44, 0x42800000, v44
	v_mul_f32_e32 v48, 0x42800000, v48
	v_mul_f32_e32 v52, 0x42800000, v52
	v_mul_f32_e32 v56, 0x42800000, v56
	v_mul_f32_e32 v60, 0x42800000, v60
	v_cvt_pk_fp8_f32 v210, v0, v4
	v_cvt_pk_fp8_f32 v211, v16, v20
	v_cvt_pk_fp8_f32 v212, v32, v36
	v_cvt_pk_fp8_f32 v213, v48, v52
	v_cvt_pk_fp8_f32 v210, v8, v12 op_sel:[0,0,1]
	v_cvt_pk_fp8_f32 v211, v24, v28 op_sel:[0,0,1]
	v_cvt_pk_fp8_f32 v212, v40, v44 op_sel:[0,0,1]
	v_cvt_pk_fp8_f32 v213, v56, v60 op_sel:[0,0,1]
	ds_write_b128 v205, v[210:213] offset:0
	v_mul_f32_e32 v1, 0x42800000, v1
	v_mul_f32_e32 v5, 0x42800000, v5
	v_mul_f32_e32 v9, 0x42800000, v9
	v_mul_f32_e32 v13, 0x42800000, v13
	v_mul_f32_e32 v17, 0x42800000, v17
	v_mul_f32_e32 v21, 0x42800000, v21
	v_mul_f32_e32 v25, 0x42800000, v25
	v_mul_f32_e32 v29, 0x42800000, v29
	v_mul_f32_e32 v33, 0x42800000, v33
	v_mul_f32_e32 v37, 0x42800000, v37
	v_mul_f32_e32 v41, 0x42800000, v41
	v_mul_f32_e32 v45, 0x42800000, v45
	v_mul_f32_e32 v49, 0x42800000, v49
	v_mul_f32_e32 v53, 0x42800000, v53
	v_mul_f32_e32 v57, 0x42800000, v57
	v_mul_f32_e32 v61, 0x42800000, v61
	v_cvt_pk_fp8_f32 v210, v1, v5
	v_cvt_pk_fp8_f32 v211, v17, v21
	v_cvt_pk_fp8_f32 v212, v33, v37
	v_cvt_pk_fp8_f32 v213, v49, v53
	v_cvt_pk_fp8_f32 v210, v9, v13 op_sel:[0,0,1]
	v_cvt_pk_fp8_f32 v211, v25, v29 op_sel:[0,0,1]
	v_cvt_pk_fp8_f32 v212, v41, v45 op_sel:[0,0,1]
	v_cvt_pk_fp8_f32 v213, v57, v61 op_sel:[0,0,1]
	ds_write_b128 v205, v[210:213] offset:128
	v_mul_f32_e32 v2, 0x42800000, v2
	v_mul_f32_e32 v6, 0x42800000, v6
	v_mul_f32_e32 v10, 0x42800000, v10
	v_mul_f32_e32 v14, 0x42800000, v14
	v_mul_f32_e32 v18, 0x42800000, v18
	v_mul_f32_e32 v22, 0x42800000, v22
	v_mul_f32_e32 v26, 0x42800000, v26
	v_mul_f32_e32 v30, 0x42800000, v30
	v_mul_f32_e32 v34, 0x42800000, v34
	v_mul_f32_e32 v38, 0x42800000, v38
	v_mul_f32_e32 v42, 0x42800000, v42
	v_mul_f32_e32 v46, 0x42800000, v46
	v_mul_f32_e32 v50, 0x42800000, v50
	v_mul_f32_e32 v54, 0x42800000, v54
	v_mul_f32_e32 v58, 0x42800000, v58
	v_mul_f32_e32 v62, 0x42800000, v62
	v_cvt_pk_fp8_f32 v210, v2, v6
	v_cvt_pk_fp8_f32 v211, v18, v22
	v_cvt_pk_fp8_f32 v212, v34, v38
	v_cvt_pk_fp8_f32 v213, v50, v54
	v_cvt_pk_fp8_f32 v210, v10, v14 op_sel:[0,0,1]
	v_cvt_pk_fp8_f32 v211, v26, v30 op_sel:[0,0,1]
	v_cvt_pk_fp8_f32 v212, v42, v46 op_sel:[0,0,1]
	v_cvt_pk_fp8_f32 v213, v58, v62 op_sel:[0,0,1]
	ds_write_b128 v205, v[210:213] offset:256
	v_mul_f32_e32 v3, 0x42800000, v3
	v_mul_f32_e32 v7, 0x42800000, v7
	v_mul_f32_e32 v11, 0x42800000, v11
	v_mul_f32_e32 v15, 0x42800000, v15
	v_mul_f32_e32 v19, 0x42800000, v19
	v_mul_f32_e32 v23, 0x42800000, v23
	v_mul_f32_e32 v27, 0x42800000, v27
	v_mul_f32_e32 v31, 0x42800000, v31
	v_mul_f32_e32 v35, 0x42800000, v35
	v_mul_f32_e32 v39, 0x42800000, v39
	v_mul_f32_e32 v43, 0x42800000, v43
	v_mul_f32_e32 v47, 0x42800000, v47
	v_mul_f32_e32 v51, 0x42800000, v51
	v_mul_f32_e32 v55, 0x42800000, v55
	v_mul_f32_e32 v59, 0x42800000, v59
	v_mul_f32_e32 v63, 0x42800000, v63
	v_cvt_pk_fp8_f32 v210, v3, v7
	v_cvt_pk_fp8_f32 v211, v19, v23
	v_cvt_pk_fp8_f32 v212, v35, v39
	v_cvt_pk_fp8_f32 v213, v51, v55
	v_cvt_pk_fp8_f32 v210, v11, v15 op_sel:[0,0,1]
	v_cvt_pk_fp8_f32 v211, v27, v31 op_sel:[0,0,1]
	v_cvt_pk_fp8_f32 v212, v43, v47 op_sel:[0,0,1]
	v_cvt_pk_fp8_f32 v213, v59, v63 op_sel:[0,0,1]
	ds_write_b128 v205, v[210:213] offset:384
	s_waitcnt lgkmcnt(0)
	s_barrier
; #define LAS __attribute__((address_space(3)))
; __device__ __forceinline__ unsigned pack4_fp8(float a, float b, float c, float d) { int r = 0; r = __builtin_amdgcn_cvt_pk_fp8_f32(a, b, r, false); r = __builtin_amdgcn_cvt_pk_fp8_f32(c, d, r, true); return (unsigned)r; }
; __device__ __forceinline__ void cvt8_to_lds(const f32x4 (&v)[16], LAS unsigned char* tile, int lane, int wv) {
; #pragma unroll
;     for (int i = 0; i < 4; ++i) { u32x4 w; w.x = pack4_fp8(v[0][i] * W8_SCALE, v[1][i] * W8_SCALE, v[2][i] * W8_SCALE, v[3][i] * W8_SCALE); w.y = pack4_fp8(v[4][i] * W8_SCALE, v[5][i] * W8_SCALE, v[6][i] * W8_SCALE, v[7][i] * W8_SCALE);
;         w.z = pack4_fp8(v[8][i] * W8_SCALE, v[9][i] * W8_SCALE, v[10][i] * W8_SCALE, v[11][i] * W8_SCALE); w.w = pack4_fp8(v[12][i] * W8_SCALE, v[13][i] * W8_SCALE, v[14][i] * W8_SCALE, v[15][i] * W8_SCALE);
;         *(LAS u32x4*)(tile + (4 * lane + i) * 128 + ((wv ^ (lane & 7)) << 4)) = w; }
; }
; __device__ __forceinline__ void cvt8_from_lds(const LAS unsigned char* tile, fp8_t* d, int ld_dst, int tid) {
;     const int c = tid & 7;
; #pragma unroll
;     for (int q = 0; q < 4; ++q) { const int r = (tid >> 3) + 64 * q; const u32x4 w = *(const LAS u32x4*)(tile + r * 128 + ((c ^ ((r >> 2) & 7)) << 4));
;         __builtin_nontemporal_store(w, (u32x4*)(d + (size_t)r * ld_dst + 16 * c)); }
; }
; __device__ __forceinline__ void cvt_item_lds(const float* src, int ld_src, fp8_t* dst, int ld_dst, LAS unsigned char* lds, int tid, int wv) {
;     const int lane = tid & 63;
;     const float* s = src + (size_t)(16 * wv) * ld_src + 4 * lane;
;     f32x4 va[16], vb[16];
;     cvt8_load(va, s, ld_src);
; #pragma unroll
;     for (int t = 0; t < 8; t += 2) {
;         cvt8_load(vb, s + (t + 1) * 256, ld_src); __builtin_amdgcn_sched_barrier(0);
;         cvt8_to_lds(va, lds, lane, wv); CVT_LDS_BAR(); __builtin_amdgcn_sched_barrier(0);
;         cvt8_from_lds(lds, dst + (size_t)(t * 256) * ld_dst, ld_dst, tid); __builtin_amdgcn_sched_barrier(0);
;         if (t + 2 < 8) { cvt8_load(va, s + (t + 2) * 256, ld_src); __builtin_amdgcn_sched_barrier(0); }
;         cvt8_to_lds(vb, lds + 32768, lane, wv); CVT_LDS_BAR(); __builtin_amdgcn_sched_barrier(0);
;         cvt8_from_lds(lds + 32768, dst + (size_t)((t + 1) * 256) * ld_dst, ld_dst, tid); __builtin_amdgcn_sched_barrier(0);
	ds_read_b128 v[0:3], v206
	ds_read_b128 v[4:7], v207
	ds_read_b128 v[8:11], v208
	ds_read_b128 v[12:15], v209
	v_add_u32_e32 v16, v140, v138
	v_add_u32_e32 v17, v142, v138
	v_add_u32_e32 v18, v144, v138
	v_add_u32_e32 v19, v146, v138
	s_waitcnt lgkmcnt(3)
	global_store_dwordx4 v16, v[0:3], s[64:65] nt
	s_waitcnt lgkmcnt(2)
	global_store_dwordx4 v17, v[4:7], s[64:65] nt
	s_waitcnt lgkmcnt(1)
	global_store_dwordx4 v18, v[8:11], s[64:65] nt
	s_waitcnt lgkmcnt(0)
	global_store_dwordx4 v19, v[12:15], s[64:65] nt
	s_add_u32 s64, s64, 0x80000
	s_addc_u32 s65, s65, 0
	s_waitcnt vmcnt(8)
	v_mul_f32_e32 v64, 0x42800000, v64
	v_mul_f32_e32 v68, 0x42800000, v68
	v_mul_f32_e32 v72, 0x42800000, v72
	v_mul_f32_e32 v76, 0x42800000, v76
	v_mul_f32_e32 v80, 0x42800000, v80
	v_mul_f32_e32 v84, 0x42800000, v84
	v_mul_f32_e32 v88, 0x42800000, v88
	v_mul_f32_e32 v92, 0x42800000, v92
	v_mul_f32_e32 v96, 0x42800000, v96
	v_mul_f32_e32 v100, 0x42800000, v100
	v_mul_f32_e32 v104, 0x42800000, v104
	v_mul_f32_e32 v108, 0x42800000, v108
	v_mul_f32_e32 v112, 0x42800000, v112
	v_mul_f32_e32 v116, 0x42800000, v116
	v_mul_f32_e32 v120, 0x42800000, v120
	v_mul_f32_e32 v124, 0x42800000, v124
	v_cvt_pk_fp8_f32 v210, v64, v68
	v_cvt_pk_fp8_f32 v211, v80, v84
	v_cvt_pk_fp8_f32 v212, v96, v100
	v_cvt_pk_fp8_f32 v213, v112, v116
	v_cvt_pk_fp8_f32 v210, v72, v76 op_sel:[0,0,1]
	v_cvt_pk_fp8_f32 v211, v88, v92 op_sel:[0,0,1]
	v_cvt_pk_fp8_f32 v212, v104, v108 op_sel:[0,0,1]
	v_cvt_pk_fp8_f32 v213, v120, v124 op_sel:[0,0,1]
	ds_write_b128 v205, v[210:213] offset:32768
	v_mul_f32_e32 v65, 0x42800000, v65
	v_mul_f32_e32 v69, 0x42800000, v69
	v_mul_f32_e32 v73, 0x42800000, v73
	v_mul_f32_e32 v77, 0x42800000, v77
	v_mul_f32_e32 v81, 0x42800000, v81
	v_mul_f32_e32 v85, 0x42800000, v85
	v_mul_f32_e32 v89, 0x42800000, v89
	v_mul_f32_e32 v93, 0x42800000, v93
	v_mul_f32_e32 v97, 0x42800000, v97
	v_mul_f32_e32 v101, 0x42800000, v101
	v_mul_f32_e32 v105, 0x42800000, v105
	v_mul_f32_e32 v109, 0x42800000, v109
	v_mul_f32_e32 v113, 0x42800000, v113
	v_mul_f32_e32 v117, 0x42800000, v117
	v_mul_f32_e32 v121, 0x42800000, v121
	v_mul_f32_e32 v125, 0x42800000, v125
	v_cvt_pk_fp8_f32 v210, v65, v69
	v_cvt_pk_fp8_f32 v211, v81, v85
	v_cvt_pk_fp8_f32 v212, v97, v101
	v_cvt_pk_fp8_f32 v213, v113, v117
	v_cvt_pk_fp8_f32 v210, v73, v77 op_sel:[0,0,1]
	v_cvt_pk_fp8_f32 v211, v89, v93 op_sel:[0,0,1]
	v_cvt_pk_fp8_f32 v212, v105, v109 op_sel:[0,0,1]
	v_cvt_pk_fp8_f32 v213, v121, v125 op_sel:[0,0,1]
	ds_write_b128 v205, v[210:213] offset:32896
	v_mul_f32_e32 v66, 0x42800000, v66
	v_mul_f32_e32 v70, 0x42800000, v70
	v_mul_f32_e32 v74, 0x42800000, v74
	v_mul_f32_e32 v78, 0x42800000, v78
	v_mul_f32_e32 v82, 0x42800000, v82
	v_mul_f32_e32 v86, 0x42800000, v86
	v_mul_f32_e32 v90, 0x42800000, v90
	v_mul_f32_e32 v94, 0x42800000, v94
	v_mul_f32_e32 v98, 0x42800000, v98
	v_mul_f32_e32 v102, 0x42800000, v102
	v_mul_f32_e32 v106, 0x42800000, v106
	v_mul_f32_e32 v110, 0x42800000, v110
	v_mul_f32_e32 v114, 0x42800000, v114
	v_mul_f32_e32 v118, 0x42800000, v118
	v_mul_f32_e32 v122, 0x42800000, v122
	v_mul_f32_e32 v126, 0x42800000, v126
	v_cvt_pk_fp8_f32 v210, v66, v70
	v_cvt_pk_fp8_f32 v211, v82, v86
	v_cvt_pk_fp8_f32 v212, v98, v102
	v_cvt_pk_fp8_f32 v213, v114, v118
	v_cvt_pk_fp8_f32 v210, v74, v78 op_sel:[0,0,1]
	v_cvt_pk_fp8_f32 v211, v90, v94 op_sel:[0,0,1]
	v_cvt_pk_fp8_f32 v212, v106, v110 op_sel:[0,0,1]
	v_cvt_pk_fp8_f32 v213, v122, v126 op_sel:[0,0,1]
	ds_write_b128 v205, v[210:213] offset:33024
	v_mul_f32_e32 v67, 0x42800000, v67
	v_mul_f32_e32 v71, 0x42800000, v71
	v_mul_f32_e32 v75, 0x42800000, v75
	v_mul_f32_e32 v79, 0x42800000, v79
	v_mul_f32_e32 v83, 0x42800000, v83
	v_mul_f32_e32 v87, 0x42800000, v87
	v_mul_f32_e32 v91, 0x42800000, v91
	v_mul_f32_e32 v95, 0x42800000, v95
	v_mul_f32_e32 v99, 0x42800000, v99
	v_mul_f32_e32 v103, 0x42800000, v103
	v_mul_f32_e32 v107, 0x42800000, v107
	v_mul_f32_e32 v111, 0x42800000, v111
	v_mul_f32_e32 v115, 0x42800000, v115
	v_mul_f32_e32 v119, 0x42800000, v119
	v_mul_f32_e32 v123, 0x42800000, v123
	v_mul_f32_e32 v127, 0x42800000, v127
	v_cvt_pk_fp8_f32 v210, v67, v71
	v_cvt_pk_fp8_f32 v211, v83, v87
	v_cvt_pk_fp8_f32 v212, v99, v103
	v_cvt_pk_fp8_f32 v213, v115, v119
	v_cvt_pk_fp8_f32 v210, v75, v79 op_sel:[0,0,1]
	v_cvt_pk_fp8_f32 v211, v91, v95 op_sel:[0,0,1]
	v_cvt_pk_fp8_f32 v212, v107, v111 op_sel:[0,0,1]
	v_cvt_pk_fp8_f32 v213, v123, v127 op_sel:[0,0,1]
	ds_write_b128 v205, v[210:213] offset:33152
	s_waitcnt lgkmcnt(0)
	s_barrier
	ds_read_b128 v[64:67], v206 offset:32768
	ds_read_b128 v[68:71], v207 offset:32768
	ds_read_b128 v[72:75], v208 offset:32768
	ds_read_b128 v[76:79], v209 offset:32768
	v_add_u32_e32 v80, v140, v138
	v_add_u32_e32 v81, v142, v138
	v_add_u32_e32 v82, v144, v138
	v_add_u32_e32 v83, v146, v138
	s_waitcnt lgkmcnt(3)
	global_store_dwordx4 v80, v[64:67], s[64:65] nt
	s_waitcnt lgkmcnt(2)
	global_store_dwordx4 v81, v[68:71], s[64:65] nt
	s_waitcnt lgkmcnt(1)
	global_store_dwordx4 v82, v[72:75], s[64:65] nt
	s_waitcnt lgkmcnt(0)
	global_store_dwordx4 v83, v[76:79], s[64:65] nt
	s_mov_b64 s[50:51], 0
